# v95 + nt on the P12 final-pass row re-reads and output stores (each touched once more, last accesses of the kernel)
# speedup vs baseline: 1.0295x; 1.0295x over previous
; #define P12_VISSUE(c_, i_, q_, D_X) do { _Pragma("unroll") for (int b = 0; b < 8; ++b) { const int idx = ((q_) * 8 + b) * 4 + eg; const unsigned ro = (unsigned)(c_) * 16384u + (unsigned)EL[(i_) * 128 + idx]; \
;           const v3u_ ld_ = *(const v3u_*)(V8 + (size_t)(ro * 192u + 12u * (unsigned)cl)); if (b & 1) D_X[b >> 1].hi = ld_; else D_X[b >> 1].lo = ld_; } } while (0)
; __device__ __forceinline__ void p12_peer(Frame& F) {
;     ...
;       v6u_ dA[4], dB[4];
;       P12_VISSUE(0, 0, 0, dA);
; _Pragma("nounroll")
;       for (int c = 0; c < 16; ++c) {
;           int lo_ = 16 * cl + 4 * eg; asm volatile("" : "+v"(lo_));
; _Pragma("nounroll")
;           for (int i = 0; i < 4; ++i) { const int t = F.gw + i * F.NGW;
;               f32x2 acc2[8];
; #pragma unroll
;               for (int m = 0; m < 8; ++m) acc2[m] = (f32x2){0.f, 0.f};
;               const v2u hb = *(const v2u*)(HN + ((size_t)t * D_ + (size_t)(unsigned)(256 * c + lo_)));
;               P12_VISSUE(c, i, 1, dB); asm volatile("" ::: "memory"); P12_VCOMP(i, 0, dA);
;               P12_VISSUE(c, i, 2, dA); asm volatile("" ::: "memory"); P12_VCOMP(i, 1, dB);
;               P12_VISSUE(c, i, 3, dB); asm volatile("" ::: "memory"); P12_VCOMP(i, 2, dA);
;               { const int in_ = i + 1 < 4 ? i + 1 : 0, cn_ = i + 1 < 4 ? c : (c + 1 < 16 ? c + 1 : 15); P12_VISSUE(cn_, in_, 0, dA); } asm volatile("" ::: "memory"); P12_VCOMP(i, 3, dB);
.LBB0_3403:
	v_add_u32_e32 v152, s28, v175
	ds_read_u16 v2, v152
	ds_read_u16 v3, v152 offset:8
	ds_read_u16 v4, v152 offset:16
	ds_read_u16 v5, v152 offset:24
	ds_read_u16 v6, v152 offset:32
	ds_read_u16 v7, v152 offset:40
	ds_read_u16 v8, v152 offset:48
	ds_read_u16 v9, v152 offset:56
	s_ashr_i32 s13, s12, 31
	s_lshl_b64 s[14:15], s[12:13], 13
	v_lshl_add_u64 v[0:1], v[164:165], 0, s[14:15]
	s_cmpk_eq_i32 s28, 0x300
	global_load_dwordx2 v[158:159], v[0:1], off
	s_cselect_b32 s30, 0, s23
	s_waitcnt lgkmcnt(7)
	v_add_u32_e32 v0, s21, v2
	v_lshl_add_u32 v179, s30, 1, v161
	s_waitcnt lgkmcnt(6)
	v_add_u32_e32 v2, s21, v3
	s_waitcnt lgkmcnt(5)
	v_add_u32_e32 v4, s21, v4
	s_waitcnt lgkmcnt(4)
	v_add_u32_e32 v10, s21, v5
	s_waitcnt lgkmcnt(3)
	v_add_u32_e32 v11, s21, v6
	s_waitcnt lgkmcnt(2)
	v_add_u32_e32 v12, s21, v7
	s_waitcnt lgkmcnt(1)
	v_add_u32_e32 v13, s21, v8
	s_waitcnt lgkmcnt(0)
	v_add_u32_e32 v14, s21, v9
	v_mad_u64_u32 v[0:1], s[30:31], v0, s16, v[160:161]
	v_mad_u64_u32 v[2:3], s[30:31], v2, s16, v[160:161]
	v_mad_u64_u32 v[4:5], s[30:31], v4, s16, v[160:161]
	v_mad_u64_u32 v[6:7], s[30:31], v10, s16, v[160:161]
	v_mad_u64_u32 v[8:9], s[30:31], v11, s16, v[160:161]
	v_mad_u64_u32 v[10:11], s[30:31], v12, s16, v[160:161]
	v_mad_u64_u32 v[12:13], s[30:31], v13, s16, v[160:161]
	v_mad_u64_u32 v[14:15], s[30:31], v14, s16, v[160:161]
	global_load_dwordx3 v[154:156], v0, s[2:3]
	global_load_dwordx3 v[220:222], v2, s[2:3]
	global_load_dwordx3 v[180:182], v4, s[2:3]
	global_load_dwordx3 v[224:226], v6, s[2:3]
	global_load_dwordx3 v[186:188], v8, s[2:3]
	global_load_dwordx3 v[228:230], v10, s[2:3]
	global_load_dwordx3 v[192:194], v12, s[2:3]
	global_load_dwordx3 v[232:234], v14, s[2:3]
	ds_read2_b32 v[166:167], v177 offset1:4
	ds_read2_b32 v[168:169], v177 offset0:8 offset1:12
	s_waitcnt vmcnt(10)
	ds_read2_b32 v[184:185], v177 offset0:16 offset1:20
	s_waitcnt vmcnt(9)
	ds_read2_b32 v[190:191], v177 offset0:24 offset1:28
	v_cvt_scalef32_pk32_f32_fp6 v[96:127], v[134:139], 1.0
	v_cvt_scalef32_pk32_f32_fp6 v[64:95], v[128:133], 1.0
	ds_read_u16 v129, v152 offset:64
	ds_read_u16 v131, v152 offset:72
	ds_read_u16 v132, v152 offset:80
	ds_read_u16 v133, v152 offset:88
	ds_read_u16 v134, v152 offset:96
	ds_read_u16 v135, v152 offset:104
	ds_read_u16 v136, v152 offset:112
	ds_read_u16 v137, v152 offset:120
	s_waitcnt lgkmcnt(11)
	v_pk_fma_f32 v[96:97], v[96:97], v[166:167], 0 op_sel_hi:[1,0,0]
	v_pk_fma_f32 v[98:99], v[98:99], v[166:167], 0 op_sel_hi:[1,0,0]
	v_pk_fma_f32 v[100:101], v[100:101], v[166:167], 0 op_sel_hi:[1,0,0]
	v_pk_fma_f32 v[102:103], v[102:103], v[166:167], 0 op_sel_hi:[1,0,0]
	v_pk_fma_f32 v[104:105], v[104:105], v[166:167], 0 op_sel_hi:[1,0,0]
	v_pk_fma_f32 v[106:107], v[106:107], v[166:167], 0 op_sel_hi:[1,0,0]
	v_pk_fma_f32 v[108:109], v[108:109], v[166:167], 0 op_sel_hi:[1,0,0]
	v_pk_fma_f32 v[110:111], v[110:111], v[166:167], 0 op_sel_hi:[1,0,0]
	v_mov_b32_e32 v128, v167
	s_waitcnt lgkmcnt(7)
	v_pk_fma_f32 v[96:97], v[112:113], v[128:129], v[96:97] op_sel_hi:[1,0,1]
	v_pk_fma_f32 v[98:99], v[114:115], v[128:129], v[98:99] op_sel_hi:[1,0,1]
	v_pk_fma_f32 v[100:101], v[116:117], v[128:129], v[100:101] op_sel_hi:[1,0,1]
	v_pk_fma_f32 v[102:103], v[118:119], v[128:129], v[102:103] op_sel_hi:[1,0,1]
	v_pk_fma_f32 v[104:105], v[120:121], v[128:129], v[104:105] op_sel_hi:[1,0,1]
	v_pk_fma_f32 v[106:107], v[122:123], v[128:129], v[106:107] op_sel_hi:[1,0,1]
	v_pk_fma_f32 v[108:109], v[124:125], v[128:129], v[108:109] op_sel_hi:[1,0,1]
	v_pk_fma_f32 v[110:111], v[126:127], v[128:129], v[110:111] op_sel_hi:[1,0,1]
	v_add_u32_e32 v112, s21, v129
	v_mov_b32_e32 v130, v169
	s_waitcnt lgkmcnt(6)
	v_add_u32_e32 v113, s21, v131
	s_waitcnt lgkmcnt(5)
	v_add_u32_e32 v114, s21, v132
	s_waitcnt lgkmcnt(4)
	v_add_u32_e32 v115, s21, v133
	s_waitcnt lgkmcnt(3)
	v_add_u32_e32 v116, s21, v134
	s_waitcnt lgkmcnt(2)
	v_add_u32_e32 v117, s21, v135
	s_waitcnt lgkmcnt(1)
	v_add_u32_e32 v118, s21, v136
	s_waitcnt lgkmcnt(0)
	v_add_u32_e32 v119, s21, v137
	v_pk_fma_f32 v[64:65], v[64:65], v[168:169], v[96:97] op_sel_hi:[1,0,1]
	v_pk_fma_f32 v[66:67], v[66:67], v[168:169], v[98:99] op_sel_hi:[1,0,1]
	v_pk_fma_f32 v[68:69], v[68:69], v[168:169], v[100:101] op_sel_hi:[1,0,1]
	v_pk_fma_f32 v[70:71], v[70:71], v[168:169], v[102:103] op_sel_hi:[1,0,1]
	v_pk_fma_f32 v[72:73], v[72:73], v[168:169], v[104:105] op_sel_hi:[1,0,1]
	v_pk_fma_f32 v[74:75], v[74:75], v[168:169], v[106:107] op_sel_hi:[1,0,1]
	v_pk_fma_f32 v[76:77], v[76:77], v[168:169], v[108:109] op_sel_hi:[1,0,1]
	v_pk_fma_f32 v[78:79], v[78:79], v[168:169], v[110:111] op_sel_hi:[1,0,1]
	v_mad_u64_u32 v[96:97], s[30:31], v112, s16, v[160:161]
	v_cvt_scalef32_pk32_f32_fp6 v[32:63], v[140:145], 1.0
	v_mad_u64_u32 v[98:99], s[30:31], v113, s16, v[160:161]
	v_mad_u64_u32 v[100:101], s[30:31], v114, s16, v[160:161]
	v_mad_u64_u32 v[102:103], s[30:31], v115, s16, v[160:161]
	v_mad_u64_u32 v[104:105], s[30:31], v116, s16, v[160:161]
	v_mad_u64_u32 v[106:107], s[30:31], v117, s16, v[160:161]
	v_mad_u64_u32 v[108:109], s[30:31], v118, s16, v[160:161]
	v_mad_u64_u32 v[110:111], s[30:31], v119, s16, v[160:161]
	v_pk_fma_f32 v[64:65], v[80:81], v[130:131], v[64:65] op_sel_hi:[1,0,1]
	v_pk_fma_f32 v[66:67], v[82:83], v[130:131], v[66:67] op_sel_hi:[1,0,1]
	v_pk_fma_f32 v[68:69], v[84:85], v[130:131], v[68:69] op_sel_hi:[1,0,1]
	v_pk_fma_f32 v[70:71], v[86:87], v[130:131], v[70:71] op_sel_hi:[1,0,1]
	v_pk_fma_f32 v[72:73], v[88:89], v[130:131], v[72:73] op_sel_hi:[1,0,1]
	v_pk_fma_f32 v[74:75], v[90:91], v[130:131], v[74:75] op_sel_hi:[1,0,1]
	v_pk_fma_f32 v[76:77], v[92:93], v[130:131], v[76:77] op_sel_hi:[1,0,1]
; #define P12_VISSUE(c_, i_, q_, D_X) do { _Pragma("unroll") for (int b = 0; b < 8; ++b) { const int idx = ((q_) * 8 + b) * 4 + eg; const unsigned ro = (unsigned)(c_) * 16384u + (unsigned)EL[(i_) * 128 + idx]; \
;           const v3u_ ld_ = *(const v3u_*)(V8 + (size_t)(ro * 192u + 12u * (unsigned)cl)); if (b & 1) D_X[b >> 1].hi = ld_; else D_X[b >> 1].lo = ld_; } } while (0)
; __device__ __forceinline__ void p12_peer(Frame& F) {
;     ...
;       v6u_ dA[4], dB[4];
;       P12_VISSUE(0, 0, 0, dA);
; _Pragma("nounroll")
;       for (int c = 0; c < 16; ++c) {
;           int lo_ = 16 * cl + 4 * eg; asm volatile("" : "+v"(lo_));
; _Pragma("nounroll")
;           for (int i = 0; i < 4; ++i) { const int t = F.gw + i * F.NGW;
;               f32x2 acc2[8];
; #pragma unroll
;               for (int m = 0; m < 8; ++m) acc2[m] = (f32x2){0.f, 0.f};
;               const v2u hb = *(const v2u*)(HN + ((size_t)t * D_ + (size_t)(unsigned)(256 * c + lo_)));
;               P12_VISSUE(c, i, 1, dB); asm volatile("" ::: "memory"); P12_VCOMP(i, 0, dA);
;               P12_VISSUE(c, i, 2, dA); asm volatile("" ::: "memory"); P12_VCOMP(i, 1, dB);
;               P12_VISSUE(c, i, 3, dB); asm volatile("" ::: "memory"); P12_VCOMP(i, 2, dA);
;               { const int in_ = i + 1 < 4 ? i + 1 : 0, cn_ = i + 1 < 4 ? c : (c + 1 < 16 ? c + 1 : 15); P12_VISSUE(cn_, in_, 0, dA); } asm volatile("" ::: "memory"); P12_VCOMP(i, 3, dB);
	v_pk_fma_f32 v[78:79], v[94:95], v[130:131], v[78:79] op_sel_hi:[1,0,1]
	global_load_dwordx3 v[198:200], v96, s[2:3]
	global_load_dwordx3 v[128:130], v98, s[2:3]
	global_load_dwordx3 v[204:206], v100, s[2:3]
	global_load_dwordx3 v[132:134], v102, s[2:3]
	global_load_dwordx3 v[210:212], v104, s[2:3]
	global_load_dwordx3 v[136:138], v106, s[2:3]
	global_load_dwordx3 v[216:218], v108, s[2:3]
	global_load_dwordx3 v[140:142], v110, s[2:3]
	v_mov_b32_e32 v144, v185
	v_pk_fma_f32 v[32:33], v[32:33], v[184:185], v[64:65] op_sel_hi:[1,0,1]
	v_pk_fma_f32 v[34:35], v[34:35], v[184:185], v[66:67] op_sel_hi:[1,0,1]
	v_pk_fma_f32 v[36:37], v[36:37], v[184:185], v[68:69] op_sel_hi:[1,0,1]
	v_pk_fma_f32 v[38:39], v[38:39], v[184:185], v[70:71] op_sel_hi:[1,0,1]
	v_pk_fma_f32 v[40:41], v[40:41], v[184:185], v[72:73] op_sel_hi:[1,0,1]
	v_pk_fma_f32 v[42:43], v[42:43], v[184:185], v[74:75] op_sel_hi:[1,0,1]
	v_pk_fma_f32 v[44:45], v[44:45], v[184:185], v[76:77] op_sel_hi:[1,0,1]
	v_pk_fma_f32 v[46:47], v[46:47], v[184:185], v[78:79] op_sel_hi:[1,0,1]
	v_cvt_scalef32_pk32_f32_fp6 v[0:31], v[146:151], 1.0
	v_pk_fma_f32 v[32:33], v[48:49], v[144:145], v[32:33] op_sel_hi:[1,0,1]
	v_pk_fma_f32 v[34:35], v[50:51], v[144:145], v[34:35] op_sel_hi:[1,0,1]
	v_pk_fma_f32 v[36:37], v[52:53], v[144:145], v[36:37] op_sel_hi:[1,0,1]
	v_pk_fma_f32 v[38:39], v[54:55], v[144:145], v[38:39] op_sel_hi:[1,0,1]
	v_pk_fma_f32 v[40:41], v[56:57], v[144:145], v[40:41] op_sel_hi:[1,0,1]
	v_pk_fma_f32 v[42:43], v[58:59], v[144:145], v[42:43] op_sel_hi:[1,0,1]
	v_pk_fma_f32 v[44:45], v[60:61], v[144:145], v[44:45] op_sel_hi:[1,0,1]
	v_pk_fma_f32 v[46:47], v[62:63], v[144:145], v[46:47] op_sel_hi:[1,0,1]
	s_waitcnt vmcnt(16)
	v_lshlrev_b32_e32 v167, 16, v159
	v_lshlrev_b32_e32 v166, 16, v158
	v_and_b32_e32 v169, 0xffff0000, v159
	v_and_b32_e32 v168, 0xffff0000, v158
	s_waitcnt vmcnt(14)
	v_mov_b32_e32 v157, v220
	v_mov_b32_e32 v158, v221
	v_mov_b32_e32 v159, v222
	v_mov_b32_e32 v146, v191
	v_pk_fma_f32 v[0:1], v[0:1], v[190:191], v[32:33] op_sel_hi:[1,0,1]
	v_pk_fma_f32 v[2:3], v[2:3], v[190:191], v[34:35] op_sel_hi:[1,0,1]
	v_pk_fma_f32 v[4:5], v[4:5], v[190:191], v[36:37] op_sel_hi:[1,0,1]
	v_pk_fma_f32 v[6:7], v[6:7], v[190:191], v[38:39] op_sel_hi:[1,0,1]
	v_pk_fma_f32 v[8:9], v[8:9], v[190:191], v[40:41] op_sel_hi:[1,0,1]
	v_pk_fma_f32 v[10:11], v[10:11], v[190:191], v[42:43] op_sel_hi:[1,0,1]
	v_pk_fma_f32 v[12:13], v[12:13], v[190:191], v[44:45] op_sel_hi:[1,0,1]
	v_pk_fma_f32 v[14:15], v[14:15], v[190:191], v[46:47] op_sel_hi:[1,0,1]
	s_waitcnt vmcnt(12)
	v_mov_b32_e32 v183, v224
	v_mov_b32_e32 v184, v225
	v_mov_b32_e32 v185, v226
	s_waitcnt vmcnt(10)
	v_mov_b32_e32 v189, v228
	v_mov_b32_e32 v190, v229
	v_mov_b32_e32 v191, v230
	s_waitcnt vmcnt(8)
	v_mov_b32_e32 v195, v232
	v_mov_b32_e32 v196, v233
	v_mov_b32_e32 v197, v234
	ds_read2_b32 v[220:221], v177 offset0:32 offset1:36
	ds_read2_b32 v[222:223], v177 offset0:40 offset1:44
	ds_read2_b32 v[242:243], v177 offset0:48 offset1:52
	ds_read2_b32 v[244:245], v177 offset0:56 offset1:60
	v_cvt_scalef32_pk32_f32_fp6 v[96:127], v[154:159], 1.0
	ds_read_u16 v131, v152 offset:128
	ds_read_u16 v135, v152 offset:136
	ds_read_u16 v139, v152 offset:144
	ds_read_u16 v143, v152 offset:152
	ds_read_u16 v153, v152 offset:160
	ds_read_u16 v154, v152 offset:168
	ds_read_u16 v155, v152 offset:176
	ds_read_u16 v152, v152 offset:184
	v_pk_fma_f32 v[144:145], v[16:17], v[146:147], v[0:1] op_sel_hi:[1,0,1]
	v_pk_fma_f32 v[148:149], v[18:19], v[146:147], v[2:3] op_sel_hi:[1,0,1]
	v_pk_fma_f32 v[150:151], v[20:21], v[146:147], v[4:5] op_sel_hi:[1,0,1]
	v_pk_fma_f32 v[202:203], v[22:23], v[146:147], v[6:7] op_sel_hi:[1,0,1]
	v_pk_fma_f32 v[208:209], v[24:25], v[146:147], v[8:9] op_sel_hi:[1,0,1]
	v_pk_fma_f32 v[214:215], v[26:27], v[146:147], v[10:11] op_sel_hi:[1,0,1]
	v_pk_fma_f32 v[236:237], v[28:29], v[146:147], v[12:13] op_sel_hi:[1,0,1]
	v_pk_fma_f32 v[146:147], v[30:31], v[146:147], v[14:15] op_sel_hi:[1,0,1]
	s_waitcnt lgkmcnt(11)
	v_pk_fma_f32 v[96:97], v[96:97], v[220:221], v[144:145] op_sel_hi:[1,0,1]
	v_mov_b32_e32 v144, v221
	v_cvt_scalef32_pk32_f32_fp6 v[64:95], v[180:185], 1.0
	v_pk_fma_f32 v[98:99], v[98:99], v[220:221], v[148:149] op_sel_hi:[1,0,1]
	v_pk_fma_f32 v[100:101], v[100:101], v[220:221], v[150:151] op_sel_hi:[1,0,1]
	v_pk_fma_f32 v[102:103], v[102:103], v[220:221], v[202:203] op_sel_hi:[1,0,1]
	v_pk_fma_f32 v[104:105], v[104:105], v[220:221], v[208:209] op_sel_hi:[1,0,1]
	v_pk_fma_f32 v[106:107], v[106:107], v[220:221], v[214:215] op_sel_hi:[1,0,1]
	v_pk_fma_f32 v[108:109], v[108:109], v[220:221], v[236:237] op_sel_hi:[1,0,1]
	v_pk_fma_f32 v[110:111], v[110:111], v[220:221], v[146:147] op_sel_hi:[1,0,1]
	v_pk_fma_f32 v[96:97], v[112:113], v[144:145], v[96:97] op_sel_hi:[1,0,1]
	s_waitcnt lgkmcnt(7)
	v_add_u32_e32 v112, s21, v131
	v_pk_fma_f32 v[98:99], v[114:115], v[144:145], v[98:99] op_sel_hi:[1,0,1]
	v_pk_fma_f32 v[100:101], v[116:117], v[144:145], v[100:101] op_sel_hi:[1,0,1]
	v_pk_fma_f32 v[102:103], v[118:119], v[144:145], v[102:103] op_sel_hi:[1,0,1]
	v_pk_fma_f32 v[104:105], v[120:121], v[144:145], v[104:105] op_sel_hi:[1,0,1]
	v_pk_fma_f32 v[106:107], v[122:123], v[144:145], v[106:107] op_sel_hi:[1,0,1]
	v_pk_fma_f32 v[108:109], v[124:125], v[144:145], v[108:109] op_sel_hi:[1,0,1]
	v_pk_fma_f32 v[110:111], v[126:127], v[144:145], v[110:111] op_sel_hi:[1,0,1]
	s_waitcnt lgkmcnt(6)
	v_add_u32_e32 v113, s21, v135
	s_waitcnt lgkmcnt(5)
	v_add_u32_e32 v114, s21, v139
	s_waitcnt lgkmcnt(4)
	v_add_u32_e32 v115, s21, v143
	s_waitcnt lgkmcnt(3)
	v_add_u32_e32 v116, s21, v153
	s_waitcnt lgkmcnt(2)
; #define P12_VISSUE(c_, i_, q_, D_X) do { _Pragma("unroll") for (int b = 0; b < 8; ++b) { const int idx = ((q_) * 8 + b) * 4 + eg; const unsigned ro = (unsigned)(c_) * 16384u + (unsigned)EL[(i_) * 128 + idx]; \
;           const v3u_ ld_ = *(const v3u_*)(V8 + (size_t)(ro * 192u + 12u * (unsigned)cl)); if (b & 1) D_X[b >> 1].hi = ld_; else D_X[b >> 1].lo = ld_; } } while (0)
; __device__ __forceinline__ void p12_peer(Frame& F) {
;     ...
;       v6u_ dA[4], dB[4];
;       P12_VISSUE(0, 0, 0, dA);
; _Pragma("nounroll")
;       for (int c = 0; c < 16; ++c) {
;           int lo_ = 16 * cl + 4 * eg; asm volatile("" : "+v"(lo_));
; _Pragma("nounroll")
;           for (int i = 0; i < 4; ++i) { const int t = F.gw + i * F.NGW;
;               f32x2 acc2[8];
; #pragma unroll
;               for (int m = 0; m < 8; ++m) acc2[m] = (f32x2){0.f, 0.f};
;               const v2u hb = *(const v2u*)(HN + ((size_t)t * D_ + (size_t)(unsigned)(256 * c + lo_)));
;               P12_VISSUE(c, i, 1, dB); asm volatile("" ::: "memory"); P12_VCOMP(i, 0, dA);
;               P12_VISSUE(c, i, 2, dA); asm volatile("" ::: "memory"); P12_VCOMP(i, 1, dB);
;               P12_VISSUE(c, i, 3, dB); asm volatile("" ::: "memory"); P12_VCOMP(i, 2, dA);
;               { const int in_ = i + 1 < 4 ? i + 1 : 0, cn_ = i + 1 < 4 ? c : (c + 1 < 16 ? c + 1 : 15); P12_VISSUE(cn_, in_, 0, dA); } asm volatile("" ::: "memory"); P12_VCOMP(i, 3, dB);
	v_add_u32_e32 v117, s21, v154
	s_waitcnt lgkmcnt(1)
	v_add_u32_e32 v118, s21, v155
	s_waitcnt lgkmcnt(0)
	v_add_u32_e32 v119, s21, v152
	v_pk_fma_f32 v[64:65], v[64:65], v[222:223], v[96:97] op_sel_hi:[1,0,1]
	v_mad_u64_u32 v[96:97], s[30:31], v112, s16, v[160:161]
	v_cvt_scalef32_pk32_f32_fp6 v[32:63], v[186:191], 1.0
	v_cvt_scalef32_pk32_f32_fp6 v[0:31], v[192:197], 1.0
	v_mov_b32_e32 v146, v223
	v_pk_fma_f32 v[66:67], v[66:67], v[222:223], v[98:99] op_sel_hi:[1,0,1]
	v_pk_fma_f32 v[68:69], v[68:69], v[222:223], v[100:101] op_sel_hi:[1,0,1]
	v_pk_fma_f32 v[70:71], v[70:71], v[222:223], v[102:103] op_sel_hi:[1,0,1]
	v_pk_fma_f32 v[72:73], v[72:73], v[222:223], v[104:105] op_sel_hi:[1,0,1]
	v_pk_fma_f32 v[74:75], v[74:75], v[222:223], v[106:107] op_sel_hi:[1,0,1]
	v_pk_fma_f32 v[76:77], v[76:77], v[222:223], v[108:109] op_sel_hi:[1,0,1]
	v_pk_fma_f32 v[78:79], v[78:79], v[222:223], v[110:111] op_sel_hi:[1,0,1]
	v_mad_u64_u32 v[98:99], s[30:31], v113, s16, v[160:161]
	v_mad_u64_u32 v[100:101], s[30:31], v114, s16, v[160:161]
	v_mad_u64_u32 v[102:103], s[30:31], v115, s16, v[160:161]
	v_mad_u64_u32 v[104:105], s[30:31], v116, s16, v[160:161]
	v_mad_u64_u32 v[106:107], s[30:31], v117, s16, v[160:161]
	v_mad_u64_u32 v[108:109], s[30:31], v118, s16, v[160:161]
	v_mad_u64_u32 v[110:111], s[30:31], v119, s16, v[160:161]
	global_load_dwordx3 v[180:182], v96, s[2:3]
	global_load_dwordx3 v[226:228], v98, s[2:3]
	global_load_dwordx3 v[186:188], v100, s[2:3]
	global_load_dwordx3 v[230:232], v102, s[2:3]
	global_load_dwordx3 v[192:194], v104, s[2:3]
	global_load_dwordx3 v[234:236], v106, s[2:3]
	global_load_dwordx3 v[222:224], v108, s[2:3]
	global_load_dwordx3 v[238:240], v110, s[2:3]
	s_waitcnt vmcnt(14)
	v_mov_b32_e32 v201, v128
	v_mov_b32_e32 v202, v129
	v_mov_b32_e32 v203, v130
	s_waitcnt vmcnt(12)
	v_mov_b32_e32 v207, v132
	v_mov_b32_e32 v208, v133
	v_mov_b32_e32 v209, v134
	s_waitcnt vmcnt(10)
	v_mov_b32_e32 v213, v136
	v_mov_b32_e32 v214, v137
	v_mov_b32_e32 v215, v138
	s_waitcnt vmcnt(8)
	v_mov_b32_e32 v219, v140
	v_mov_b32_e32 v220, v141
	v_mov_b32_e32 v221, v142
	v_pk_fma_f32 v[64:65], v[80:81], v[146:147], v[64:65] op_sel_hi:[1,0,1]
	v_pk_fma_f32 v[66:67], v[82:83], v[146:147], v[66:67] op_sel_hi:[1,0,1]
	v_pk_fma_f32 v[68:69], v[84:85], v[146:147], v[68:69] op_sel_hi:[1,0,1]
	v_pk_fma_f32 v[70:71], v[86:87], v[146:147], v[70:71] op_sel_hi:[1,0,1]
	v_pk_fma_f32 v[72:73], v[88:89], v[146:147], v[72:73] op_sel_hi:[1,0,1]
	v_pk_fma_f32 v[74:75], v[90:91], v[146:147], v[74:75] op_sel_hi:[1,0,1]
	v_pk_fma_f32 v[76:77], v[92:93], v[146:147], v[76:77] op_sel_hi:[1,0,1]
	v_pk_fma_f32 v[78:79], v[94:95], v[146:147], v[78:79] op_sel_hi:[1,0,1]
	ds_read2_b32 v[196:197], v177 offset0:64 offset1:68
	v_mov_b32_e32 v184, v243
	ds_read2_b32 v[246:247], v177 offset0:72 offset1:76
	ds_read2_b32 v[248:249], v177 offset0:80 offset1:84
	ds_read2_b32 v[250:251], v177 offset0:88 offset1:92
	v_pk_fma_f32 v[32:33], v[32:33], v[242:243], v[64:65] op_sel_hi:[1,0,1]
	v_pk_fma_f32 v[34:35], v[34:35], v[242:243], v[66:67] op_sel_hi:[1,0,1]
	v_pk_fma_f32 v[36:37], v[36:37], v[242:243], v[68:69] op_sel_hi:[1,0,1]
	v_pk_fma_f32 v[38:39], v[38:39], v[242:243], v[70:71] op_sel_hi:[1,0,1]
	v_pk_fma_f32 v[40:41], v[40:41], v[242:243], v[72:73] op_sel_hi:[1,0,1]
	v_pk_fma_f32 v[42:43], v[42:43], v[242:243], v[74:75] op_sel_hi:[1,0,1]
	v_pk_fma_f32 v[44:45], v[44:45], v[242:243], v[76:77] op_sel_hi:[1,0,1]
	v_pk_fma_f32 v[46:47], v[46:47], v[242:243], v[78:79] op_sel_hi:[1,0,1]
	v_cvt_scalef32_pk32_f32_fp6 v[128:159], v[198:203], 1.0
	v_cvt_scalef32_pk32_f32_fp6 v[96:127], v[204:209], 1.0
	v_cvt_scalef32_pk32_f32_fp6 v[64:95], v[210:215], 1.0
	v_pk_fma_f32 v[198:199], v[48:49], v[184:185], v[32:33] op_sel_hi:[1,0,1]
	v_pk_fma_f32 v[200:201], v[50:51], v[184:185], v[34:35] op_sel_hi:[1,0,1]
	v_pk_fma_f32 v[202:203], v[52:53], v[184:185], v[36:37] op_sel_hi:[1,0,1]
	v_pk_fma_f32 v[204:205], v[54:55], v[184:185], v[38:39] op_sel_hi:[1,0,1]
	v_pk_fma_f32 v[206:207], v[56:57], v[184:185], v[40:41] op_sel_hi:[1,0,1]
	v_pk_fma_f32 v[208:209], v[58:59], v[184:185], v[42:43] op_sel_hi:[1,0,1]
	v_pk_fma_f32 v[210:211], v[60:61], v[184:185], v[44:45] op_sel_hi:[1,0,1]
	v_pk_fma_f32 v[184:185], v[62:63], v[184:185], v[46:47] op_sel_hi:[1,0,1]
	ds_read_u16 v183, v179 offset:16384
	ds_read_u16 v189, v179 offset:16392
	ds_read_u16 v191, v179 offset:16400
	ds_read_u16 v195, v179 offset:16408
	ds_read_u16 v212, v179 offset:16416
	ds_read_u16 v213, v179 offset:16424
	ds_read_u16 v214, v179 offset:16432
	ds_read_u16 v179, v179 offset:16440
	v_mov_b32_e32 v190, v245
	v_pk_fma_f32 v[0:1], v[0:1], v[244:245], v[198:199] op_sel_hi:[1,0,1]
	v_pk_fma_f32 v[2:3], v[2:3], v[244:245], v[200:201] op_sel_hi:[1,0,1]
	v_pk_fma_f32 v[4:5], v[4:5], v[244:245], v[202:203] op_sel_hi:[1,0,1]
	v_pk_fma_f32 v[6:7], v[6:7], v[244:245], v[204:205] op_sel_hi:[1,0,1]
	v_pk_fma_f32 v[8:9], v[8:9], v[244:245], v[206:207] op_sel_hi:[1,0,1]
	v_pk_fma_f32 v[10:11], v[10:11], v[244:245], v[208:209] op_sel_hi:[1,0,1]
	v_pk_fma_f32 v[12:13], v[12:13], v[244:245], v[210:211] op_sel_hi:[1,0,1]
	v_pk_fma_f32 v[14:15], v[14:15], v[244:245], v[184:185] op_sel_hi:[1,0,1]
	s_cselect_b32 s29, s22, s17
	s_waitcnt lgkmcnt(5)
; #define P12_VISSUE(c_, i_, q_, D_X) do { _Pragma("unroll") for (int b = 0; b < 8; ++b) { const int idx = ((q_) * 8 + b) * 4 + eg; const unsigned ro = (unsigned)(c_) * 16384u + (unsigned)EL[(i_) * 128 + idx]; \
;           const v3u_ ld_ = *(const v3u_*)(V8 + (size_t)(ro * 192u + 12u * (unsigned)cl)); if (b & 1) D_X[b >> 1].hi = ld_; else D_X[b >> 1].lo = ld_; } } while (0)
; __device__ __forceinline__ void p12_peer(Frame& F) {
;     ...
;       v6u_ dA[4], dB[4];
;       P12_VISSUE(0, 0, 0, dA);
; _Pragma("nounroll")
;       for (int c = 0; c < 16; ++c) {
;           int lo_ = 16 * cl + 4 * eg; asm volatile("" : "+v"(lo_));
; _Pragma("nounroll")
;           for (int i = 0; i < 4; ++i) { const int t = F.gw + i * F.NGW;
;               f32x2 acc2[8];
; #pragma unroll
;               for (int m = 0; m < 8; ++m) acc2[m] = (f32x2){0.f, 0.f};
;               const v2u hb = *(const v2u*)(HN + ((size_t)t * D_ + (size_t)(unsigned)(256 * c + lo_)));
;               P12_VISSUE(c, i, 1, dB); asm volatile("" ::: "memory"); P12_VCOMP(i, 0, dA);
;               P12_VISSUE(c, i, 2, dA); asm volatile("" ::: "memory"); P12_VCOMP(i, 1, dB);
;               P12_VISSUE(c, i, 3, dB); asm volatile("" ::: "memory"); P12_VCOMP(i, 2, dA);
;               { const int in_ = i + 1 < 4 ? i + 1 : 0, cn_ = i + 1 < 4 ? c : (c + 1 < 16 ? c + 1 : 15); P12_VISSUE(cn_, in_, 0, dA); } asm volatile("" ::: "memory"); P12_VCOMP(i, 3, dB);
	v_pk_fma_f32 v[0:1], v[16:17], v[190:191], v[0:1] op_sel_hi:[1,0,1]
	v_pk_fma_f32 v[2:3], v[18:19], v[190:191], v[2:3] op_sel_hi:[1,0,1]
	v_pk_fma_f32 v[4:5], v[20:21], v[190:191], v[4:5] op_sel_hi:[1,0,1]
	v_pk_fma_f32 v[6:7], v[22:23], v[190:191], v[6:7] op_sel_hi:[1,0,1]
	v_pk_fma_f32 v[8:9], v[24:25], v[190:191], v[8:9] op_sel_hi:[1,0,1]
	v_pk_fma_f32 v[10:11], v[26:27], v[190:191], v[10:11] op_sel_hi:[1,0,1]
	v_pk_fma_f32 v[12:13], v[28:29], v[190:191], v[12:13] op_sel_hi:[1,0,1]
	v_pk_fma_f32 v[14:15], v[30:31], v[190:191], v[14:15] op_sel_hi:[1,0,1]
	s_lshl_b64 s[14:15], s[12:13], 14
	s_lshl_b32 s13, s29, 14
	v_pk_fma_f32 v[0:1], v[128:129], v[196:197], v[0:1] op_sel_hi:[1,0,1]
	v_pk_fma_f32 v[2:3], v[130:131], v[196:197], v[2:3] op_sel_hi:[1,0,1]
	v_pk_fma_f32 v[4:5], v[132:133], v[196:197], v[4:5] op_sel_hi:[1,0,1]
	v_pk_fma_f32 v[6:7], v[134:135], v[196:197], v[6:7] op_sel_hi:[1,0,1]
	v_pk_fma_f32 v[8:9], v[136:137], v[196:197], v[8:9] op_sel_hi:[1,0,1]
	v_pk_fma_f32 v[10:11], v[138:139], v[196:197], v[10:11] op_sel_hi:[1,0,1]
	v_pk_fma_f32 v[12:13], v[140:141], v[196:197], v[12:13] op_sel_hi:[1,0,1]
	v_pk_fma_f32 v[14:15], v[142:143], v[196:197], v[14:15] op_sel_hi:[1,0,1]
	v_mov_b32_e32 v16, v197
	v_pk_fma_f32 v[0:1], v[144:145], v[16:17], v[0:1] op_sel_hi:[1,0,1]
	v_pk_fma_f32 v[2:3], v[146:147], v[16:17], v[2:3] op_sel_hi:[1,0,1]
	v_pk_fma_f32 v[4:5], v[148:149], v[16:17], v[4:5] op_sel_hi:[1,0,1]
	v_pk_fma_f32 v[6:7], v[150:151], v[16:17], v[6:7] op_sel_hi:[1,0,1]
	v_pk_fma_f32 v[8:9], v[152:153], v[16:17], v[8:9] op_sel_hi:[1,0,1]
	v_pk_fma_f32 v[10:11], v[154:155], v[16:17], v[10:11] op_sel_hi:[1,0,1]
	v_pk_fma_f32 v[12:13], v[156:157], v[16:17], v[12:13] op_sel_hi:[1,0,1]
	v_pk_fma_f32 v[14:15], v[158:159], v[16:17], v[14:15] op_sel_hi:[1,0,1]
	v_add_u32_e32 v16, s13, v183
	v_add_u32_e32 v19, s13, v189
	v_add_u32_e32 v21, s13, v191
	s_waitcnt lgkmcnt(4)
	v_add_u32_e32 v23, s13, v195
	s_waitcnt lgkmcnt(3)
	v_add_u32_e32 v30, s13, v212
	s_waitcnt lgkmcnt(2)
	v_add_u32_e32 v128, s13, v213
	s_waitcnt lgkmcnt(1)
	v_add_u32_e32 v129, s13, v214
	s_waitcnt lgkmcnt(0)
	v_add_u32_e32 v130, s13, v179
	v_mad_u64_u32 v[16:17], s[30:31], v16, s16, v[160:161]
	v_pk_fma_f32 v[0:1], v[96:97], v[246:247], v[0:1] op_sel_hi:[1,0,1]
	v_pk_fma_f32 v[2:3], v[98:99], v[246:247], v[2:3] op_sel_hi:[1,0,1]
	v_pk_fma_f32 v[4:5], v[100:101], v[246:247], v[4:5] op_sel_hi:[1,0,1]
	v_mad_u64_u32 v[24:25], s[30:31], v19, s16, v[160:161]
	v_mad_u64_u32 v[26:27], s[30:31], v21, s16, v[160:161]
	v_mad_u64_u32 v[28:29], s[30:31], v23, s16, v[160:161]
	v_mad_u64_u32 v[30:31], s[30:31], v30, s16, v[160:161]
	v_mad_u64_u32 v[96:97], s[30:31], v128, s16, v[160:161]
	v_mad_u64_u32 v[98:99], s[30:31], v129, s16, v[160:161]
	v_mad_u64_u32 v[100:101], s[30:31], v130, s16, v[160:161]
	global_load_dwordx3 v[134:136], v16, s[2:3]
	global_load_dwordx3 v[152:154], v24, s[2:3]
	global_load_dwordx3 v[128:130], v26, s[2:3]
	global_load_dwordx3 v[156:158], v28, s[2:3]
	global_load_dwordx3 v[140:142], v30, s[2:3]
	global_load_dwordx3 v[198:200], v96, s[2:3]
	global_load_dwordx3 v[146:148], v98, s[2:3]
	global_load_dwordx3 v[202:204], v100, s[2:3]
	v_mov_b32_e32 v18, v247
	v_pk_fma_f32 v[6:7], v[102:103], v[246:247], v[6:7] op_sel_hi:[1,0,1]
	v_pk_fma_f32 v[8:9], v[104:105], v[246:247], v[8:9] op_sel_hi:[1,0,1]
	v_pk_fma_f32 v[10:11], v[106:107], v[246:247], v[10:11] op_sel_hi:[1,0,1]
	v_pk_fma_f32 v[12:13], v[108:109], v[246:247], v[12:13] op_sel_hi:[1,0,1]
	v_pk_fma_f32 v[14:15], v[110:111], v[246:247], v[14:15] op_sel_hi:[1,0,1]
	s_waitcnt vmcnt(14)
	v_mov_b32_e32 v183, v226
	v_mov_b32_e32 v184, v227
	v_mov_b32_e32 v185, v228
	v_pk_fma_f32 v[0:1], v[112:113], v[18:19], v[0:1] op_sel_hi:[1,0,1]
	v_pk_fma_f32 v[2:3], v[114:115], v[18:19], v[2:3] op_sel_hi:[1,0,1]
	v_pk_fma_f32 v[4:5], v[116:117], v[18:19], v[4:5] op_sel_hi:[1,0,1]
	v_pk_fma_f32 v[6:7], v[118:119], v[18:19], v[6:7] op_sel_hi:[1,0,1]
	v_pk_fma_f32 v[8:9], v[120:121], v[18:19], v[8:9] op_sel_hi:[1,0,1]
	v_pk_fma_f32 v[10:11], v[122:123], v[18:19], v[10:11] op_sel_hi:[1,0,1]
	v_pk_fma_f32 v[12:13], v[124:125], v[18:19], v[12:13] op_sel_hi:[1,0,1]
	v_pk_fma_f32 v[14:15], v[126:127], v[18:19], v[14:15] op_sel_hi:[1,0,1]
	ds_read2_b32 v[214:215], v177 offset0:96 offset1:100
	v_mov_b32_e32 v20, v249
	v_pk_fma_f32 v[0:1], v[64:65], v[248:249], v[0:1] op_sel_hi:[1,0,1]
	v_pk_fma_f32 v[2:3], v[66:67], v[248:249], v[2:3] op_sel_hi:[1,0,1]
	v_pk_fma_f32 v[4:5], v[68:69], v[248:249], v[4:5] op_sel_hi:[1,0,1]
	v_pk_fma_f32 v[6:7], v[70:71], v[248:249], v[6:7] op_sel_hi:[1,0,1]
	v_pk_fma_f32 v[8:9], v[72:73], v[248:249], v[8:9] op_sel_hi:[1,0,1]
	v_pk_fma_f32 v[10:11], v[74:75], v[248:249], v[10:11] op_sel_hi:[1,0,1]
	v_pk_fma_f32 v[12:13], v[76:77], v[248:249], v[12:13] op_sel_hi:[1,0,1]
	v_pk_fma_f32 v[14:15], v[78:79], v[248:249], v[14:15] op_sel_hi:[1,0,1]
	s_waitcnt vmcnt(12)
	v_mov_b32_e32 v189, v230
	v_mov_b32_e32 v190, v231
	v_mov_b32_e32 v191, v232
	v_cvt_scalef32_pk32_f32_fp6 v[32:63], v[216:221], 1.0
	v_pk_fma_f32 v[0:1], v[80:81], v[20:21], v[0:1] op_sel_hi:[1,0,1]
	v_pk_fma_f32 v[2:3], v[82:83], v[20:21], v[2:3] op_sel_hi:[1,0,1]
	v_pk_fma_f32 v[4:5], v[84:85], v[20:21], v[4:5] op_sel_hi:[1,0,1]
	v_pk_fma_f32 v[6:7], v[86:87], v[20:21], v[6:7] op_sel_hi:[1,0,1]
	v_pk_fma_f32 v[8:9], v[88:89], v[20:21], v[8:9] op_sel_hi:[1,0,1]
	v_pk_fma_f32 v[10:11], v[90:91], v[20:21], v[10:11] op_sel_hi:[1,0,1]
	v_pk_fma_f32 v[12:13], v[92:93], v[20:21], v[12:13] op_sel_hi:[1,0,1]
	v_pk_fma_f32 v[14:15], v[94:95], v[20:21], v[14:15] op_sel_hi:[1,0,1]
	ds_read2_b32 v[216:217], v177 offset0:104 offset1:108
	v_mov_b32_e32 v22, v251
	v_pk_fma_f32 v[0:1], v[32:33], v[250:251], v[0:1] op_sel_hi:[1,0,1]
	v_pk_fma_f32 v[2:3], v[34:35], v[250:251], v[2:3] op_sel_hi:[1,0,1]
	v_pk_fma_f32 v[4:5], v[36:37], v[250:251], v[4:5] op_sel_hi:[1,0,1]
	v_pk_fma_f32 v[6:7], v[38:39], v[250:251], v[6:7] op_sel_hi:[1,0,1]
	v_pk_fma_f32 v[8:9], v[40:41], v[250:251], v[8:9] op_sel_hi:[1,0,1]
	v_pk_fma_f32 v[10:11], v[42:43], v[250:251], v[10:11] op_sel_hi:[1,0,1]
	v_pk_fma_f32 v[12:13], v[44:45], v[250:251], v[12:13] op_sel_hi:[1,0,1]
	v_pk_fma_f32 v[14:15], v[46:47], v[250:251], v[14:15] op_sel_hi:[1,0,1]
	s_waitcnt vmcnt(10)
; #define P12_VISSUE(c_, i_, q_, D_X) do { _Pragma("unroll") for (int b = 0; b < 8; ++b) { const int idx = ((q_) * 8 + b) * 4 + eg; const unsigned ro = (unsigned)(c_) * 16384u + (unsigned)EL[(i_) * 128 + idx]; \
;           const v3u_ ld_ = *(const v3u_*)(V8 + (size_t)(ro * 192u + 12u * (unsigned)cl)); if (b & 1) D_X[b >> 1].hi = ld_; else D_X[b >> 1].lo = ld_; } } while (0)
; __device__ __forceinline__ void p12_peer(Frame& F) {
;     ...
;       v6u_ dA[4], dB[4];
;       P12_VISSUE(0, 0, 0, dA);
; _Pragma("nounroll")
;       for (int c = 0; c < 16; ++c) {
;           int lo_ = 16 * cl + 4 * eg; asm volatile("" : "+v"(lo_));
; _Pragma("nounroll")
;           for (int i = 0; i < 4; ++i) { const int t = F.gw + i * F.NGW;
;               f32x2 acc2[8];
; #pragma unroll
;               for (int m = 0; m < 8; ++m) acc2[m] = (f32x2){0.f, 0.f};
;               const v2u hb = *(const v2u*)(HN + ((size_t)t * D_ + (size_t)(unsigned)(256 * c + lo_)));
;               P12_VISSUE(c, i, 1, dB); asm volatile("" ::: "memory"); P12_VCOMP(i, 0, dA);
;               P12_VISSUE(c, i, 2, dA); asm volatile("" ::: "memory"); P12_VCOMP(i, 1, dB);
;               P12_VISSUE(c, i, 3, dB); asm volatile("" ::: "memory"); P12_VCOMP(i, 2, dA);
;               { const int in_ = i + 1 < 4 ? i + 1 : 0, cn_ = i + 1 < 4 ? c : (c + 1 < 16 ? c + 1 : 15); P12_VISSUE(cn_, in_, 0, dA); } asm volatile("" ::: "memory"); P12_VCOMP(i, 3, dB);
;               float r8[8], r4[4];
; #pragma unroll
;               for (int m = 0; m < 8; ++m) { const float lo_v = (m & 1) ? acc2[m >> 1].y : acc2[m >> 1].x, hi_v = (m & 1) ? acc2[4 + (m >> 1)].y : acc2[4 + (m >> 1)].x;
;                   const float keep = hi5 ? hi_v : lo_v, send = hi5 ? lo_v : hi_v;
;                   r8[m] = keep + __builtin_bit_cast(float, __builtin_amdgcn_ds_bpermute((F.lane ^ 32) << 2, __builtin_bit_cast(int, send))); }
; #pragma unroll
;               for (int m = 0; m < 4; ++m) { const float keep = hi4 ? r8[4 + m] : r8[m], send = hi4 ? r8[m] : r8[4 + m];
;                   r4[m] = keep + __builtin_bit_cast(float, __builtin_amdgcn_ds_bpermute((F.lane ^ 16) << 2, __builtin_bit_cast(int, send))); }
;               int lo3_ = lo_; asm volatile("" : "+v"(lo3_));
;               const size_t col = (size_t)t * D_ + (size_t)(unsigned)(256 * c + lo3_);
	v_mov_b32_e32 v195, v234
	v_mov_b32_e32 v196, v235
	v_mov_b32_e32 v197, v236
	v_mov_b32_e32 v162, v176
	v_pk_fma_f32 v[132:133], v[48:49], v[22:23], v[0:1] op_sel_hi:[1,0,1]
	v_pk_fma_f32 v[138:139], v[50:51], v[22:23], v[2:3] op_sel_hi:[1,0,1]
	v_pk_fma_f32 v[144:145], v[52:53], v[22:23], v[4:5] op_sel_hi:[1,0,1]
	v_pk_fma_f32 v[150:151], v[54:55], v[22:23], v[6:7] op_sel_hi:[1,0,1]
	v_pk_fma_f32 v[206:207], v[56:57], v[22:23], v[8:9] op_sel_hi:[1,0,1]
	v_pk_fma_f32 v[208:209], v[58:59], v[22:23], v[10:11] op_sel_hi:[1,0,1]
	v_pk_fma_f32 v[210:211], v[60:61], v[22:23], v[12:13] op_sel_hi:[1,0,1]
	v_pk_fma_f32 v[212:213], v[62:63], v[22:23], v[14:15] op_sel_hi:[1,0,1]
	s_waitcnt vmcnt(8)
	v_mov_b32_e32 v225, v238
	v_mov_b32_e32 v226, v239
	v_mov_b32_e32 v227, v240
	ds_read2_b32 v[218:219], v177 offset0:112 offset1:116
	v_cvt_scalef32_pk32_f32_fp6 v[96:127], v[180:185], 1.0
	s_add_u32 s14, s26, s14
	ds_read2_b32 v[220:221], v177 offset0:120 offset1:124
	s_waitcnt lgkmcnt(3)
	v_pk_fma_f32 v[96:97], v[96:97], v[214:215], v[132:133] op_sel_hi:[1,0,1]
	v_pk_fma_f32 v[98:99], v[98:99], v[214:215], v[138:139] op_sel_hi:[1,0,1]
	v_pk_fma_f32 v[100:101], v[100:101], v[214:215], v[144:145] op_sel_hi:[1,0,1]
	v_pk_fma_f32 v[102:103], v[102:103], v[214:215], v[150:151] op_sel_hi:[1,0,1]
	v_pk_fma_f32 v[104:105], v[104:105], v[214:215], v[206:207] op_sel_hi:[1,0,1]
	v_pk_fma_f32 v[106:107], v[106:107], v[214:215], v[208:209] op_sel_hi:[1,0,1]
	v_pk_fma_f32 v[108:109], v[108:109], v[214:215], v[210:211] op_sel_hi:[1,0,1]
	v_pk_fma_f32 v[110:111], v[110:111], v[214:215], v[212:213] op_sel_hi:[1,0,1]
	v_mov_b32_e32 v132, v215
	s_addc_u32 s15, s27, s15
	v_cvt_scalef32_pk32_f32_fp6 v[64:95], v[186:191], 1.0
	v_add_u32_e32 v162, s18, v162
	v_pk_fma_f32 v[96:97], v[112:113], v[132:133], v[96:97] op_sel_hi:[1,0,1]
	v_pk_fma_f32 v[98:99], v[114:115], v[132:133], v[98:99] op_sel_hi:[1,0,1]
	v_pk_fma_f32 v[100:101], v[116:117], v[132:133], v[100:101] op_sel_hi:[1,0,1]
	v_pk_fma_f32 v[102:103], v[118:119], v[132:133], v[102:103] op_sel_hi:[1,0,1]
	v_pk_fma_f32 v[104:105], v[120:121], v[132:133], v[104:105] op_sel_hi:[1,0,1]
	v_pk_fma_f32 v[106:107], v[122:123], v[132:133], v[106:107] op_sel_hi:[1,0,1]
	v_pk_fma_f32 v[108:109], v[124:125], v[132:133], v[108:109] op_sel_hi:[1,0,1]
	v_pk_fma_f32 v[110:111], v[126:127], v[132:133], v[110:111] op_sel_hi:[1,0,1]
	v_lshl_add_u64 v[180:181], v[162:163], 2, s[14:15]
	s_waitcnt lgkmcnt(2)
	v_mov_b32_e32 v162, v217
	v_pk_fma_f32 v[64:65], v[64:65], v[216:217], v[96:97] op_sel_hi:[1,0,1]
	v_pk_fma_f32 v[66:67], v[66:67], v[216:217], v[98:99] op_sel_hi:[1,0,1]
	v_pk_fma_f32 v[68:69], v[68:69], v[216:217], v[100:101] op_sel_hi:[1,0,1]
	v_pk_fma_f32 v[70:71], v[70:71], v[216:217], v[102:103] op_sel_hi:[1,0,1]
	v_pk_fma_f32 v[72:73], v[72:73], v[216:217], v[104:105] op_sel_hi:[1,0,1]
	v_pk_fma_f32 v[74:75], v[74:75], v[216:217], v[106:107] op_sel_hi:[1,0,1]
	v_pk_fma_f32 v[76:77], v[76:77], v[216:217], v[108:109] op_sel_hi:[1,0,1]
	v_pk_fma_f32 v[78:79], v[78:79], v[216:217], v[110:111] op_sel_hi:[1,0,1]
	v_cvt_scalef32_pk32_f32_fp6 v[32:63], v[192:197], 1.0
	v_pk_fma_f32 v[64:65], v[80:81], v[162:163], v[64:65] op_sel_hi:[1,0,1]
	v_pk_fma_f32 v[66:67], v[82:83], v[162:163], v[66:67] op_sel_hi:[1,0,1]
	v_pk_fma_f32 v[68:69], v[84:85], v[162:163], v[68:69] op_sel_hi:[1,0,1]
	v_pk_fma_f32 v[70:71], v[86:87], v[162:163], v[70:71] op_sel_hi:[1,0,1]
	v_pk_fma_f32 v[72:73], v[88:89], v[162:163], v[72:73] op_sel_hi:[1,0,1]
	v_pk_fma_f32 v[74:75], v[90:91], v[162:163], v[74:75] op_sel_hi:[1,0,1]
	v_pk_fma_f32 v[76:77], v[92:93], v[162:163], v[76:77] op_sel_hi:[1,0,1]
	v_pk_fma_f32 v[78:79], v[94:95], v[162:163], v[78:79] op_sel_hi:[1,0,1]
	s_waitcnt lgkmcnt(1)
	v_mov_b32_e32 v182, v219
	v_pk_fma_f32 v[32:33], v[32:33], v[218:219], v[64:65] op_sel_hi:[1,0,1]
	v_pk_fma_f32 v[34:35], v[34:35], v[218:219], v[66:67] op_sel_hi:[1,0,1]
	v_pk_fma_f32 v[36:37], v[36:37], v[218:219], v[68:69] op_sel_hi:[1,0,1]
	v_pk_fma_f32 v[38:39], v[38:39], v[218:219], v[70:71] op_sel_hi:[1,0,1]
	v_pk_fma_f32 v[40:41], v[40:41], v[218:219], v[72:73] op_sel_hi:[1,0,1]
	v_pk_fma_f32 v[42:43], v[42:43], v[218:219], v[74:75] op_sel_hi:[1,0,1]
	v_pk_fma_f32 v[44:45], v[44:45], v[218:219], v[76:77] op_sel_hi:[1,0,1]
	v_pk_fma_f32 v[46:47], v[46:47], v[218:219], v[78:79] op_sel_hi:[1,0,1]
	v_cvt_scalef32_pk32_f32_fp6 v[0:31], v[222:227], 1.0
	v_pk_fma_f32 v[32:33], v[48:49], v[182:183], v[32:33] op_sel_hi:[1,0,1]
	v_pk_fma_f32 v[34:35], v[50:51], v[182:183], v[34:35] op_sel_hi:[1,0,1]
	v_pk_fma_f32 v[36:37], v[52:53], v[182:183], v[36:37] op_sel_hi:[1,0,1]
	v_pk_fma_f32 v[38:39], v[54:55], v[182:183], v[38:39] op_sel_hi:[1,0,1]
	v_pk_fma_f32 v[40:41], v[56:57], v[182:183], v[40:41] op_sel_hi:[1,0,1]
	v_pk_fma_f32 v[42:43], v[58:59], v[182:183], v[42:43] op_sel_hi:[1,0,1]
	v_pk_fma_f32 v[44:45], v[60:61], v[182:183], v[44:45] op_sel_hi:[1,0,1]
	v_pk_fma_f32 v[46:47], v[62:63], v[182:183], v[46:47] op_sel_hi:[1,0,1]
	s_waitcnt lgkmcnt(0)
; __device__ __forceinline__ int fresh_lane() { int l; asm volatile("v_mbcnt_lo_u32_b32 %0, -1, 0\n\tv_mbcnt_hi_u32_b32 %0, -1, %0" : "=v"(l)); return l; }
; __device__ __forceinline__ float bflo(unsigned w) { return __uint_as_float(w << 16); }
; __device__ __forceinline__ float bfhi(unsigned w) { return __uint_as_float(w & 0xffff0000u); }
; __device__ __forceinline__ float wave_sum(float v) { v = dpp_add16(v); return (rdlane(v, 0) + rdlane(v, 16)) + (rdlane(v, 32) + rdlane(v, 48)); }
; __device__ __forceinline__ void p12_peer(Frame& F) {
;     ...
;               float r8[8], r4[4];
; #pragma unroll
;               for (int m = 0; m < 8; ++m) { const float lo_v = (m & 1) ? acc2[m >> 1].y : acc2[m >> 1].x, hi_v = (m & 1) ? acc2[4 + (m >> 1)].y : acc2[4 + (m >> 1)].x;
;                   const float keep = hi5 ? hi_v : lo_v, send = hi5 ? lo_v : hi_v;
;                   r8[m] = keep + __builtin_bit_cast(float, __builtin_amdgcn_ds_bpermute((F.lane ^ 32) << 2, __builtin_bit_cast(int, send))); }
; #pragma unroll
;               for (int m = 0; m < 4; ++m) { const float keep = hi4 ? r8[4 + m] : r8[m], send = hi4 ? r8[m] : r8[4 + m];
;                   r4[m] = keep + __builtin_bit_cast(float, __builtin_amdgcn_ds_bpermute((F.lane ^ 16) << 2, __builtin_bit_cast(int, send))); }
;               int lo3_ = lo_; asm volatile("" : "+v"(lo3_));
;               const size_t col = (size_t)t * D_ + (size_t)(unsigned)(256 * c + lo3_);
;               const f32x4 o = {r4[0] + bflo(hb.x), r4[1] + bfhi(hb.x), r4[2] + bflo(hb.y), r4[3] + bfhi(hb.y)};
;               SSQ[i * 64 + F.lane] += (o.x * o.x + o.y * o.y) + (o.z * o.z + o.w * o.w);
;               *(f32x4*)(F.out + col) = o;
;     ...
;       __builtin_amdgcn_fence(__ATOMIC_SEQ_CST, "agent");
;       const int l2_ = fresh_lane(), lo2_ = 16 * (l2_ & 15) + 4 * (l2_ >> 4);
; #pragma unroll
;       for (int i = 0; i < 4; ++i) { const int t = F.gw + i * F.NGW;
;           const float rs = 1.0f / sqrtf(wave_sum(SSQ[i * 64 + l2_]) * (1.f / D_) + 1e-6f);
; _Pragma("nounroll")
;           for (int c0 = 0; c0 < 16; c0 += 8) {
; #pragma unroll
;               for (int c = c0; c < c0 + 8; ++c) { const size_t col = (size_t)t * D_ + (size_t)(unsigned)(256 * c + lo2_); const f32x4 gn = *(const f32x4*)(lnf + (256 * c + lo2_));
;                   const f32x4 o = *(const f32x4*)(F.out + col);
	v_mov_b32_e32 v184, v221
	v_pk_fma_f32 v[0:1], v[0:1], v[220:221], v[32:33] op_sel_hi:[1,0,1]
	v_pk_fma_f32 v[2:3], v[2:3], v[220:221], v[34:35] op_sel_hi:[1,0,1]
	v_pk_fma_f32 v[4:5], v[4:5], v[220:221], v[36:37] op_sel_hi:[1,0,1]
	v_pk_fma_f32 v[6:7], v[6:7], v[220:221], v[38:39] op_sel_hi:[1,0,1]
	v_pk_fma_f32 v[8:9], v[8:9], v[220:221], v[40:41] op_sel_hi:[1,0,1]
	v_pk_fma_f32 v[10:11], v[10:11], v[220:221], v[42:43] op_sel_hi:[1,0,1]
	v_pk_fma_f32 v[12:13], v[12:13], v[220:221], v[44:45] op_sel_hi:[1,0,1]
	v_pk_fma_f32 v[14:15], v[14:15], v[220:221], v[46:47] op_sel_hi:[1,0,1]
	v_pk_fma_f32 v[0:1], v[16:17], v[184:185], v[0:1] op_sel_hi:[1,0,1]
	v_pk_fma_f32 v[2:3], v[18:19], v[184:185], v[2:3] op_sel_hi:[1,0,1]
	v_pk_fma_f32 v[4:5], v[20:21], v[184:185], v[4:5] op_sel_hi:[1,0,1]
	v_pk_fma_f32 v[6:7], v[22:23], v[184:185], v[6:7] op_sel_hi:[1,0,1]
	v_pk_fma_f32 v[8:9], v[24:25], v[184:185], v[8:9] op_sel_hi:[1,0,1]
	v_pk_fma_f32 v[10:11], v[26:27], v[184:185], v[10:11] op_sel_hi:[1,0,1]
	v_pk_fma_f32 v[12:13], v[28:29], v[184:185], v[12:13] op_sel_hi:[1,0,1]
	v_pk_fma_f32 v[14:15], v[30:31], v[184:185], v[14:15] op_sel_hi:[1,0,1]
	v_cndmask_b32_e32 v18, v0, v8, vcc
	v_cndmask_b32_e32 v19, v1, v9, vcc
	v_cndmask_b32_e32 v20, v2, v10, vcc
	v_cndmask_b32_e32 v21, v3, v11, vcc
	v_cndmask_b32_e32 v22, v4, v12, vcc
	v_cndmask_b32_e32 v23, v5, v13, vcc
	v_cndmask_b32_e32 v24, v6, v14, vcc
	v_cndmask_b32_e32 v25, v7, v15, vcc
	v_cndmask_b32_e32 v17, v10, v2, vcc
	v_cndmask_b32_e32 v16, v8, v0, vcc
	v_cndmask_b32_e32 v3, v11, v3, vcc
	v_cndmask_b32_e32 v2, v9, v1, vcc
	v_cndmask_b32_e32 v1, v14, v6, vcc
	v_cndmask_b32_e32 v0, v12, v4, vcc
	v_cndmask_b32_e32 v6, v13, v5, vcc
	ds_bpermute_b32 v4, v171, v18
	ds_bpermute_b32 v8, v171, v19
	ds_bpermute_b32 v5, v171, v20
	ds_bpermute_b32 v9, v171, v21
	ds_bpermute_b32 v10, v171, v22
	ds_bpermute_b32 v12, v171, v23
	ds_bpermute_b32 v11, v171, v24
	ds_bpermute_b32 v13, v171, v25
	v_cndmask_b32_e32 v7, v15, v7, vcc
	s_waitcnt lgkmcnt(5)
	v_pk_add_f32 v[4:5], v[16:17], v[4:5]
	s_waitcnt lgkmcnt(4)
	v_pk_add_f32 v[2:3], v[2:3], v[8:9]
	s_waitcnt lgkmcnt(1)
	v_pk_add_f32 v[0:1], v[0:1], v[10:11]
	s_waitcnt lgkmcnt(0)
	v_pk_add_f32 v[6:7], v[6:7], v[12:13]
	v_cndmask_b32_e64 v10, v4, v0, s[0:1]
	v_cndmask_b32_e64 v11, v2, v6, s[0:1]
	v_cndmask_b32_e64 v9, v1, v5, s[0:1]
	v_cndmask_b32_e64 v8, v0, v4, s[0:1]
	v_cndmask_b32_e64 v5, v5, v1, s[0:1]
	v_cndmask_b32_e64 v0, v6, v2, s[0:1]
	v_cndmask_b32_e64 v6, v3, v7, s[0:1]
	v_cndmask_b32_e64 v1, v7, v3, s[0:1]
	ds_bpermute_b32 v2, v170, v10
	ds_bpermute_b32 v4, v170, v11
	ds_bpermute_b32 v3, v170, v5
	ds_bpermute_b32 v5, v170, v6
	v_add_u32_e32 v178, s28, v174
	ds_read_b32 v155, v178
	s_addk_i32 s28, 0x100
	s_waitcnt lgkmcnt(2)
	v_pk_add_f32 v[2:3], v[8:9], v[2:3]
	s_waitcnt lgkmcnt(1)
	v_pk_add_f32 v[0:1], v[0:1], v[4:5]
	v_pk_add_f32 v[4:5], v[2:3], v[166:167]
	v_pk_add_f32 v[2:3], v[0:1], v[168:169]
	v_mov_b32_e32 v0, v4
	v_pk_mul_f32 v[6:7], v[2:3], v[2:3]
	v_mov_b32_e32 v1, v2
	v_mov_b32_e32 v2, v5
	v_pk_fma_f32 v[4:5], v[4:5], v[4:5], v[6:7]
	s_addk_i32 s23, 0x80
	s_add_i32 s12, s12, s34
	global_store_dwordx4 v[180:181], v[0:3], off
	s_cmpk_eq_i32 s28, 0x400
	v_add_u32_e32 v177, 0x200, v177
	v_add_f32_e32 v0, v4, v5
	s_waitcnt vmcnt(1)
	v_mov_b32_e32 v149, v202
	v_mov_b32_e32 v150, v203
	v_mov_b32_e32 v151, v204
	v_mov_b32_e32 v143, v198
	v_mov_b32_e32 v144, v199
	v_mov_b32_e32 v145, v200
	v_mov_b32_e32 v131, v156
	v_mov_b32_e32 v132, v157
	v_mov_b32_e32 v133, v158
	v_mov_b32_e32 v137, v152
	v_mov_b32_e32 v138, v153
	v_mov_b32_e32 v139, v154
	s_waitcnt lgkmcnt(0)
	v_add_f32_e32 v0, v155, v0
	ds_write_b32 v178, v0
	s_cbranch_scc0 .LBB0_3403
	s_cmp_eq_u32 s19, 16
	s_mov_b32 s17, s19
	s_cbranch_scc0 .LBB0_3402
	s_waitcnt vmcnt(0) lgkmcnt(0)
	buffer_inv sc1
	v_mbcnt_lo_u32_b32 v0, -1, 0
	v_mbcnt_hi_u32_b32 v0, -1, v0
	v_lshl_add_u32 v7, v0, 2, s20
	v_and_b32_e32 v2, 15, v0
	v_lshrrev_b32_e32 v3, 4, v0
	v_lshlrev_b32_e32 v2, 6, v2
	v_lshl_add_u32 v6, v3, 4, v2
	v_add_u32_e32 v10, 0x1000, v6
	v_add_u32_e32 v11, 0x2000, v6
	v_add_u32_e32 v12, 0x3000, v6
	s_lshl_b64 s[0:1], s[94:95], 14
	s_add_u32 s12, s26, s0
	s_addc_u32 s13, s27, s1
	s_lshl_b64 s[0:1], s[4:5], 14
	s_add_u32 s14, s26, s0
	s_addc_u32 s15, s27, s1
	s_lshl_b64 s[0:1], s[8:9], 14
	s_add_u32 s16, s26, s0
	s_addc_u32 s17, s27, s1
	s_lshl_b64 s[0:1], s[10:11], 14
	s_add_u32 s18, s26, s0
	s_addc_u32 s19, s27, s1
	global_load_dwordx4 v[60:63], v6, s[24:25] offset:0
	global_load_dwordx4 v[64:67], v6, s[24:25] offset:1024
	global_load_dwordx4 v[68:71], v6, s[24:25] offset:2048
	global_load_dwordx4 v[72:75], v6, s[24:25] offset:3072
	global_load_dwordx4 v[76:79], v10, s[24:25] offset:0
	global_load_dwordx4 v[80:83], v10, s[24:25] offset:1024
	global_load_dwordx4 v[84:87], v10, s[24:25] offset:2048
	global_load_dwordx4 v[88:91], v10, s[24:25] offset:3072
	global_load_dwordx4 v[92:95], v11, s[24:25] offset:0
	global_load_dwordx4 v[96:99], v11, s[24:25] offset:1024
	global_load_dwordx4 v[100:103], v11, s[24:25] offset:2048
	global_load_dwordx4 v[104:107], v11, s[24:25] offset:3072
	global_load_dwordx4 v[108:111], v12, s[24:25] offset:0
	global_load_dwordx4 v[112:115], v12, s[24:25] offset:1024
	global_load_dwordx4 v[116:119], v12, s[24:25] offset:2048
	global_load_dwordx4 v[120:123], v12, s[24:25] offset:3072
	global_load_dwordx4 v[124:127], v6, s[12:13] offset:0 nt
	global_load_dwordx4 v[128:131], v6, s[12:13] offset:1024 nt
	global_load_dwordx4 v[132:135], v6, s[12:13] offset:2048 nt
	global_load_dwordx4 v[136:139], v6, s[12:13] offset:3072 nt
	global_load_dwordx4 v[140:143], v10, s[12:13] offset:0 nt
; __device__ __forceinline__ float wave_sum(float v) { v = dpp_add16(v); return (rdlane(v, 0) + rdlane(v, 16)) + (rdlane(v, 32) + rdlane(v, 48)); }
; __device__ __forceinline__ void p12_peer(Frame& F) {
;     ...
;       for (int i = 0; i < 4; ++i) { const int t = F.gw + i * F.NGW;
;           const float rs = 1.0f / sqrtf(wave_sum(SSQ[i * 64 + l2_]) * (1.f / D_) + 1e-6f);
; _Pragma("nounroll")
;           for (int c0 = 0; c0 < 16; c0 += 8) {
; #pragma unroll
;               for (int c = c0; c < c0 + 8; ++c) { const size_t col = (size_t)t * D_ + (size_t)(unsigned)(256 * c + lo2_); const f32x4 gn = *(const f32x4*)(lnf + (256 * c + lo2_));
;                   const f32x4 o = *(const f32x4*)(F.out + col);
	global_load_dwordx4 v[144:147], v10, s[12:13] offset:1024 nt
	global_load_dwordx4 v[148:151], v10, s[12:13] offset:2048 nt
	global_load_dwordx4 v[152:155], v10, s[12:13] offset:3072 nt
	global_load_dwordx4 v[156:159], v11, s[12:13] offset:0 nt
	global_load_dwordx4 v[160:163], v11, s[12:13] offset:1024 nt
	global_load_dwordx4 v[164:167], v11, s[12:13] offset:2048 nt
	global_load_dwordx4 v[168:171], v11, s[12:13] offset:3072 nt
	global_load_dwordx4 v[172:175], v12, s[12:13] offset:0 nt
	global_load_dwordx4 v[176:179], v12, s[12:13] offset:1024 nt
	global_load_dwordx4 v[180:183], v12, s[12:13] offset:2048 nt
	global_load_dwordx4 v[184:187], v12, s[12:13] offset:3072 nt
	global_load_dwordx4 v[188:191], v6, s[14:15] offset:0 nt
	global_load_dwordx4 v[192:195], v6, s[14:15] offset:1024 nt
	global_load_dwordx4 v[196:199], v6, s[14:15] offset:2048 nt
	global_load_dwordx4 v[200:203], v6, s[14:15] offset:3072 nt
	global_load_dwordx4 v[204:207], v10, s[14:15] offset:0 nt
	global_load_dwordx4 v[208:211], v10, s[14:15] offset:1024 nt
	global_load_dwordx4 v[212:215], v10, s[14:15] offset:2048 nt
	global_load_dwordx4 v[216:219], v10, s[14:15] offset:3072 nt
	global_load_dwordx4 v[220:223], v11, s[14:15] offset:0 nt
	global_load_dwordx4 v[224:227], v11, s[14:15] offset:1024 nt
	global_load_dwordx4 v[228:231], v11, s[14:15] offset:2048 nt
	global_load_dwordx4 v[232:235], v11, s[14:15] offset:3072 nt
	global_load_dwordx4 v[236:239], v12, s[14:15] offset:0 nt
	global_load_dwordx4 v[240:243], v12, s[14:15] offset:1024 nt
	global_load_dwordx4 v[244:247], v12, s[14:15] offset:2048 nt
	global_load_dwordx4 v[248:251], v12, s[14:15] offset:3072 nt
	ds_read_b32 v1, v7 offset:4096
	s_waitcnt lgkmcnt(0)
	v_add_f32_dpp v1, v1, v1 quad_perm:[1,0,3,2] row_mask:0xf bank_mask:0xf bound_ctrl:1
	s_nop 1
	v_add_f32_dpp v1, v1, v1 quad_perm:[2,3,0,1] row_mask:0xf bank_mask:0xf bound_ctrl:1
	s_nop 1
	v_add_f32_dpp v1, v1, v1 row_half_mirror row_mask:0xf bank_mask:0xf bound_ctrl:1
	s_nop 1
	v_add_f32_dpp v1, v1, v1 row_mirror row_mask:0xf bank_mask:0xf bound_ctrl:1
	s_nop 0
	v_readlane_b32 s1, v1, 16
	v_readlane_b32 s0, v1, 0
	s_nop 0
	v_mov_b32_e32 v3, s1
	v_readlane_b32 s1, v1, 48
	v_add_f32_e32 v3, s0, v3
	v_readlane_b32 s0, v1, 32
	v_mov_b32_e32 v1, s1
	s_nop 0
	v_add_f32_e32 v1, s0, v1
	v_add_f32_e32 v1, v3, v1
	v_mov_b32_e32 v3, 0x358637bd
	v_fmac_f32_e32 v3, 0x39800000, v1
	s_mov_b32 s0, 0xf800000
	v_mul_f32_e32 v1, 0x4f800000, v3
	v_cmp_gt_f32_e32 vcc, s0, v3
	s_nop 1
	v_cndmask_b32_e32 v1, v3, v1, vcc
	v_sqrt_f32_e32 v3, v1
	s_nop 0
	v_add_u32_e32 v4, -1, v3
	v_fma_f32 v5, -v4, v3, v1
	v_cmp_ge_f32_e64 s[0:1], 0, v5
	v_add_u32_e32 v5, 1, v3
	s_nop 0
	v_cndmask_b32_e64 v4, v3, v4, s[0:1]
	v_fma_f32 v3, -v5, v3, v1
	v_cmp_lt_f32_e64 s[0:1], 0, v3
	s_nop 1
	v_cndmask_b32_e64 v3, v4, v5, s[0:1]
	v_mul_f32_e32 v4, 0x37800000, v3
	v_cndmask_b32_e32 v3, v3, v4, vcc
	v_mov_b32_e32 v4, 0x260
	v_cmp_class_f32_e32 vcc, v1, v4
	s_nop 1
	v_cndmask_b32_e32 v3, v3, v1, vcc
	v_div_scale_f32 v4, s[0:1], v3, v3, 1.0
	v_rcp_f32_e32 v5, v4
	s_nop 0
	v_fma_f32 v0, -v4, v5, 1.0
	v_fmac_f32_e32 v5, v0, v5
	v_div_scale_f32 v0, vcc, 1.0, v3, 1.0
	v_mul_f32_e32 v2, v0, v5
	v_fma_f32 v8, -v4, v2, v0
	v_fmac_f32_e32 v2, v8, v5
	v_fma_f32 v0, -v4, v2, v0
	v_div_fmas_f32 v0, v0, v5, v2
	v_div_fixup_f32 v2, v0, v3, 1.0
	v_mov_b32_e32 v40, v2
	v_mov_b32_e32 v41, v2
	ds_read_b32 v1, v7 offset:4352
	s_waitcnt lgkmcnt(0)
	v_add_f32_dpp v1, v1, v1 quad_perm:[1,0,3,2] row_mask:0xf bank_mask:0xf bound_ctrl:1
	s_nop 1
	v_add_f32_dpp v1, v1, v1 quad_perm:[2,3,0,1] row_mask:0xf bank_mask:0xf bound_ctrl:1
	s_nop 1
	v_add_f32_dpp v1, v1, v1 row_half_mirror row_mask:0xf bank_mask:0xf bound_ctrl:1
	s_nop 1
	v_add_f32_dpp v1, v1, v1 row_mirror row_mask:0xf bank_mask:0xf bound_ctrl:1
	s_nop 0
	v_readlane_b32 s1, v1, 16
	v_readlane_b32 s0, v1, 0
	s_nop 0
	v_mov_b32_e32 v3, s1
	v_readlane_b32 s1, v1, 48
	v_add_f32_e32 v3, s0, v3
	v_readlane_b32 s0, v1, 32
	v_mov_b32_e32 v1, s1
	s_nop 0
	v_add_f32_e32 v1, s0, v1
	v_add_f32_e32 v1, v3, v1
	v_mov_b32_e32 v3, 0x358637bd
	v_fmac_f32_e32 v3, 0x39800000, v1
	s_mov_b32 s0, 0xf800000
	v_mul_f32_e32 v1, 0x4f800000, v3
	v_cmp_gt_f32_e32 vcc, s0, v3
	s_nop 1
	v_cndmask_b32_e32 v1, v3, v1, vcc
	v_sqrt_f32_e32 v3, v1
	s_nop 0
	v_add_u32_e32 v4, -1, v3
	v_fma_f32 v5, -v4, v3, v1
	v_cmp_ge_f32_e64 s[0:1], 0, v5
	v_add_u32_e32 v5, 1, v3
	s_nop 0
	v_cndmask_b32_e64 v4, v3, v4, s[0:1]
	v_fma_f32 v3, -v5, v3, v1
	v_cmp_lt_f32_e64 s[0:1], 0, v3
	s_nop 1
	v_cndmask_b32_e64 v3, v4, v5, s[0:1]
	v_mul_f32_e32 v4, 0x37800000, v3
	v_cndmask_b32_e32 v3, v3, v4, vcc
	v_mov_b32_e32 v4, 0x260
	v_cmp_class_f32_e32 vcc, v1, v4
	s_nop 1
	v_cndmask_b32_e32 v3, v3, v1, vcc
	v_div_scale_f32 v4, s[0:1], v3, v3, 1.0
	v_rcp_f32_e32 v5, v4
	s_nop 0
	v_fma_f32 v0, -v4, v5, 1.0
	v_fmac_f32_e32 v5, v0, v5
	v_div_scale_f32 v0, vcc, 1.0, v3, 1.0
	v_mul_f32_e32 v2, v0, v5
	v_fma_f32 v8, -v4, v2, v0
	v_fmac_f32_e32 v2, v8, v5
	v_fma_f32 v0, -v4, v2, v0
	v_div_fmas_f32 v0, v0, v5, v2
	v_div_fixup_f32 v2, v0, v3, 1.0
	v_mov_b32_e32 v42, v2
	v_mov_b32_e32 v43, v2
	ds_read_b32 v1, v7 offset:4608
	s_waitcnt lgkmcnt(0)
; __device__ __forceinline__ float wave_sum(float v) { v = dpp_add16(v); return (rdlane(v, 0) + rdlane(v, 16)) + (rdlane(v, 32) + rdlane(v, 48)); }
; __device__ __forceinline__ void p12_peer(Frame& F) {
;     ...
;       for (int i = 0; i < 4; ++i) { const int t = F.gw + i * F.NGW;
;           const float rs = 1.0f / sqrtf(wave_sum(SSQ[i * 64 + l2_]) * (1.f / D_) + 1e-6f);
; _Pragma("nounroll")
;           for (int c0 = 0; c0 < 16; c0 += 8) {
; #pragma unroll
;               for (int c = c0; c < c0 + 8; ++c) { const size_t col = (size_t)t * D_ + (size_t)(unsigned)(256 * c + lo2_); const f32x4 gn = *(const f32x4*)(lnf + (256 * c + lo2_));
;                   const f32x4 o = *(const f32x4*)(F.out + col);
;                   *(f32x4*)(F.out + col) = (f32x4){o.x * rs * gn.x, o.y * rs * gn.y, o.z * rs * gn.z, o.w * rs * gn.w}; }
	v_add_f32_dpp v1, v1, v1 quad_perm:[1,0,3,2] row_mask:0xf bank_mask:0xf bound_ctrl:1
	s_nop 1
	v_add_f32_dpp v1, v1, v1 quad_perm:[2,3,0,1] row_mask:0xf bank_mask:0xf bound_ctrl:1
	s_nop 1
	v_add_f32_dpp v1, v1, v1 row_half_mirror row_mask:0xf bank_mask:0xf bound_ctrl:1
	s_nop 1
	v_add_f32_dpp v1, v1, v1 row_mirror row_mask:0xf bank_mask:0xf bound_ctrl:1
	s_nop 0
	v_readlane_b32 s1, v1, 16
	v_readlane_b32 s0, v1, 0
	s_nop 0
	v_mov_b32_e32 v3, s1
	v_readlane_b32 s1, v1, 48
	v_add_f32_e32 v3, s0, v3
	v_readlane_b32 s0, v1, 32
	v_mov_b32_e32 v1, s1
	s_nop 0
	v_add_f32_e32 v1, s0, v1
	v_add_f32_e32 v1, v3, v1
	v_mov_b32_e32 v3, 0x358637bd
	v_fmac_f32_e32 v3, 0x39800000, v1
	s_mov_b32 s0, 0xf800000
	v_mul_f32_e32 v1, 0x4f800000, v3
	v_cmp_gt_f32_e32 vcc, s0, v3
	s_nop 1
	v_cndmask_b32_e32 v1, v3, v1, vcc
	v_sqrt_f32_e32 v3, v1
	s_nop 0
	v_add_u32_e32 v4, -1, v3
	v_fma_f32 v5, -v4, v3, v1
	v_cmp_ge_f32_e64 s[0:1], 0, v5
	v_add_u32_e32 v5, 1, v3
	s_nop 0
	v_cndmask_b32_e64 v4, v3, v4, s[0:1]
	v_fma_f32 v3, -v5, v3, v1
	v_cmp_lt_f32_e64 s[0:1], 0, v3
	s_nop 1
	v_cndmask_b32_e64 v3, v4, v5, s[0:1]
	v_mul_f32_e32 v4, 0x37800000, v3
	v_cndmask_b32_e32 v3, v3, v4, vcc
	v_mov_b32_e32 v4, 0x260
	v_cmp_class_f32_e32 vcc, v1, v4
	s_nop 1
	v_cndmask_b32_e32 v3, v3, v1, vcc
	v_div_scale_f32 v4, s[0:1], v3, v3, 1.0
	v_rcp_f32_e32 v5, v4
	s_nop 0
	v_fma_f32 v0, -v4, v5, 1.0
	v_fmac_f32_e32 v5, v0, v5
	v_div_scale_f32 v0, vcc, 1.0, v3, 1.0
	v_mul_f32_e32 v2, v0, v5
	v_fma_f32 v8, -v4, v2, v0
	v_fmac_f32_e32 v2, v8, v5
	v_fma_f32 v0, -v4, v2, v0
	v_div_fmas_f32 v0, v0, v5, v2
	v_div_fixup_f32 v2, v0, v3, 1.0
	v_mov_b32_e32 v44, v2
	v_mov_b32_e32 v45, v2
	ds_read_b32 v1, v7 offset:4864
	s_waitcnt lgkmcnt(0)
	v_add_f32_dpp v1, v1, v1 quad_perm:[1,0,3,2] row_mask:0xf bank_mask:0xf bound_ctrl:1
	s_nop 1
	v_add_f32_dpp v1, v1, v1 quad_perm:[2,3,0,1] row_mask:0xf bank_mask:0xf bound_ctrl:1
	s_nop 1
	v_add_f32_dpp v1, v1, v1 row_half_mirror row_mask:0xf bank_mask:0xf bound_ctrl:1
	s_nop 1
	v_add_f32_dpp v1, v1, v1 row_mirror row_mask:0xf bank_mask:0xf bound_ctrl:1
	s_nop 0
	v_readlane_b32 s1, v1, 16
	v_readlane_b32 s0, v1, 0
	s_nop 0
	v_mov_b32_e32 v3, s1
	v_readlane_b32 s1, v1, 48
	v_add_f32_e32 v3, s0, v3
	v_readlane_b32 s0, v1, 32
	v_mov_b32_e32 v1, s1
	s_nop 0
	v_add_f32_e32 v1, s0, v1
	v_add_f32_e32 v1, v3, v1
	v_mov_b32_e32 v3, 0x358637bd
	v_fmac_f32_e32 v3, 0x39800000, v1
	s_mov_b32 s0, 0xf800000
	v_mul_f32_e32 v1, 0x4f800000, v3
	v_cmp_gt_f32_e32 vcc, s0, v3
	s_nop 1
	v_cndmask_b32_e32 v1, v3, v1, vcc
	v_sqrt_f32_e32 v3, v1
	s_nop 0
	v_add_u32_e32 v4, -1, v3
	v_fma_f32 v5, -v4, v3, v1
	v_cmp_ge_f32_e64 s[0:1], 0, v5
	v_add_u32_e32 v5, 1, v3
	s_nop 0
	v_cndmask_b32_e64 v4, v3, v4, s[0:1]
	v_fma_f32 v3, -v5, v3, v1
	v_cmp_lt_f32_e64 s[0:1], 0, v3
	s_nop 1
	v_cndmask_b32_e64 v3, v4, v5, s[0:1]
	v_mul_f32_e32 v4, 0x37800000, v3
	v_cndmask_b32_e32 v3, v3, v4, vcc
	v_mov_b32_e32 v4, 0x260
	v_cmp_class_f32_e32 vcc, v1, v4
	s_nop 1
	v_cndmask_b32_e32 v3, v3, v1, vcc
	v_div_scale_f32 v4, s[0:1], v3, v3, 1.0
	v_rcp_f32_e32 v5, v4
	s_nop 0
	v_fma_f32 v0, -v4, v5, 1.0
	v_fmac_f32_e32 v5, v0, v5
	v_div_scale_f32 v0, vcc, 1.0, v3, 1.0
	v_mul_f32_e32 v2, v0, v5
	v_fma_f32 v8, -v4, v2, v0
	v_fmac_f32_e32 v2, v8, v5
	v_fma_f32 v0, -v4, v2, v0
	v_div_fmas_f32 v0, v0, v5, v2
	v_div_fixup_f32 v2, v0, v3, 1.0
	v_mov_b32_e32 v46, v2
	v_mov_b32_e32 v47, v2
	s_waitcnt vmcnt(31)
	v_pk_mul_f32 v[124:125], v[40:41], v[124:125]
	v_pk_mul_f32 v[126:127], v[40:41], v[126:127]
	v_pk_mul_f32 v[124:125], v[60:61], v[124:125]
	v_pk_mul_f32 v[126:127], v[62:63], v[126:127]
	global_store_dwordx4 v6, v[124:127], s[12:13] offset:0 nt
	s_waitcnt vmcnt(31)
	v_pk_mul_f32 v[128:129], v[40:41], v[128:129]
	v_pk_mul_f32 v[130:131], v[40:41], v[130:131]
	v_pk_mul_f32 v[128:129], v[64:65], v[128:129]
	v_pk_mul_f32 v[130:131], v[66:67], v[130:131]
	global_store_dwordx4 v6, v[128:131], s[12:13] offset:1024 nt
	s_waitcnt vmcnt(31)
	v_pk_mul_f32 v[132:133], v[40:41], v[132:133]
	v_pk_mul_f32 v[134:135], v[40:41], v[134:135]
	v_pk_mul_f32 v[132:133], v[68:69], v[132:133]
	v_pk_mul_f32 v[134:135], v[70:71], v[134:135]
	global_store_dwordx4 v6, v[132:135], s[12:13] offset:2048 nt
	s_waitcnt vmcnt(31)
	v_pk_mul_f32 v[136:137], v[40:41], v[136:137]
	v_pk_mul_f32 v[138:139], v[40:41], v[138:139]
	v_pk_mul_f32 v[136:137], v[72:73], v[136:137]
	v_pk_mul_f32 v[138:139], v[74:75], v[138:139]
	global_store_dwordx4 v6, v[136:139], s[12:13] offset:3072 nt
	s_waitcnt vmcnt(31)
	v_pk_mul_f32 v[140:141], v[40:41], v[140:141]
	v_pk_mul_f32 v[142:143], v[40:41], v[142:143]
	v_pk_mul_f32 v[140:141], v[76:77], v[140:141]
	v_pk_mul_f32 v[142:143], v[78:79], v[142:143]
	global_store_dwordx4 v10, v[140:143], s[12:13] offset:0 nt
	s_waitcnt vmcnt(31)
	v_pk_mul_f32 v[144:145], v[40:41], v[144:145]
	v_pk_mul_f32 v[146:147], v[40:41], v[146:147]
	v_pk_mul_f32 v[144:145], v[80:81], v[144:145]
	v_pk_mul_f32 v[146:147], v[82:83], v[146:147]
	global_store_dwordx4 v10, v[144:147], s[12:13] offset:1024 nt
	s_waitcnt vmcnt(31)
	v_pk_mul_f32 v[148:149], v[40:41], v[148:149]
	v_pk_mul_f32 v[150:151], v[40:41], v[150:151]
	v_pk_mul_f32 v[148:149], v[84:85], v[148:149]
	v_pk_mul_f32 v[150:151], v[86:87], v[150:151]
	global_store_dwordx4 v10, v[148:151], s[12:13] offset:2048 nt
	s_waitcnt vmcnt(31)
	v_pk_mul_f32 v[152:153], v[40:41], v[152:153]
	v_pk_mul_f32 v[154:155], v[40:41], v[154:155]
	v_pk_mul_f32 v[152:153], v[88:89], v[152:153]
	v_pk_mul_f32 v[154:155], v[90:91], v[154:155]
	global_store_dwordx4 v10, v[152:155], s[12:13] offset:3072 nt
	s_waitcnt vmcnt(31)
; __device__ __forceinline__ float wave_sum(float v) { v = dpp_add16(v); return (rdlane(v, 0) + rdlane(v, 16)) + (rdlane(v, 32) + rdlane(v, 48)); }
; __device__ __forceinline__ void p12_peer(Frame& F) {
;     ...
;       for (int i = 0; i < 4; ++i) { const int t = F.gw + i * F.NGW;
;           const float rs = 1.0f / sqrtf(wave_sum(SSQ[i * 64 + l2_]) * (1.f / D_) + 1e-6f);
; _Pragma("nounroll")
;           for (int c0 = 0; c0 < 16; c0 += 8) {
; #pragma unroll
;               for (int c = c0; c < c0 + 8; ++c) { const size_t col = (size_t)t * D_ + (size_t)(unsigned)(256 * c + lo2_); const f32x4 gn = *(const f32x4*)(lnf + (256 * c + lo2_));
;                   const f32x4 o = *(const f32x4*)(F.out + col);
;                   *(f32x4*)(F.out + col) = (f32x4){o.x * rs * gn.x, o.y * rs * gn.y, o.z * rs * gn.z, o.w * rs * gn.w}; }
;               asm volatile("" ::: "memory"); } }
	v_pk_mul_f32 v[156:157], v[40:41], v[156:157]
	v_pk_mul_f32 v[158:159], v[40:41], v[158:159]
	v_pk_mul_f32 v[156:157], v[92:93], v[156:157]
	v_pk_mul_f32 v[158:159], v[94:95], v[158:159]
	global_store_dwordx4 v11, v[156:159], s[12:13] offset:0 nt
	s_waitcnt vmcnt(31)
	v_pk_mul_f32 v[160:161], v[40:41], v[160:161]
	v_pk_mul_f32 v[162:163], v[40:41], v[162:163]
	v_pk_mul_f32 v[160:161], v[96:97], v[160:161]
	v_pk_mul_f32 v[162:163], v[98:99], v[162:163]
	global_store_dwordx4 v11, v[160:163], s[12:13] offset:1024 nt
	s_waitcnt vmcnt(31)
	v_pk_mul_f32 v[164:165], v[40:41], v[164:165]
	v_pk_mul_f32 v[166:167], v[40:41], v[166:167]
	v_pk_mul_f32 v[164:165], v[100:101], v[164:165]
	v_pk_mul_f32 v[166:167], v[102:103], v[166:167]
	global_store_dwordx4 v11, v[164:167], s[12:13] offset:2048 nt
	s_waitcnt vmcnt(31)
	v_pk_mul_f32 v[168:169], v[40:41], v[168:169]
	v_pk_mul_f32 v[170:171], v[40:41], v[170:171]
	v_pk_mul_f32 v[168:169], v[104:105], v[168:169]
	v_pk_mul_f32 v[170:171], v[106:107], v[170:171]
	global_store_dwordx4 v11, v[168:171], s[12:13] offset:3072 nt
	s_waitcnt vmcnt(31)
	v_pk_mul_f32 v[172:173], v[40:41], v[172:173]
	v_pk_mul_f32 v[174:175], v[40:41], v[174:175]
	v_pk_mul_f32 v[172:173], v[108:109], v[172:173]
	v_pk_mul_f32 v[174:175], v[110:111], v[174:175]
	global_store_dwordx4 v12, v[172:175], s[12:13] offset:0 nt
	s_waitcnt vmcnt(31)
	v_pk_mul_f32 v[176:177], v[40:41], v[176:177]
	v_pk_mul_f32 v[178:179], v[40:41], v[178:179]
	v_pk_mul_f32 v[176:177], v[112:113], v[176:177]
	v_pk_mul_f32 v[178:179], v[114:115], v[178:179]
	global_store_dwordx4 v12, v[176:179], s[12:13] offset:1024 nt
	s_waitcnt vmcnt(31)
	v_pk_mul_f32 v[180:181], v[40:41], v[180:181]
	v_pk_mul_f32 v[182:183], v[40:41], v[182:183]
	v_pk_mul_f32 v[180:181], v[116:117], v[180:181]
	v_pk_mul_f32 v[182:183], v[118:119], v[182:183]
	global_store_dwordx4 v12, v[180:183], s[12:13] offset:2048 nt
	s_waitcnt vmcnt(31)
	v_pk_mul_f32 v[184:185], v[40:41], v[184:185]
	v_pk_mul_f32 v[186:187], v[40:41], v[186:187]
	v_pk_mul_f32 v[184:185], v[120:121], v[184:185]
	v_pk_mul_f32 v[186:187], v[122:123], v[186:187]
	global_store_dwordx4 v12, v[184:187], s[12:13] offset:3072 nt
	s_nop 1
	global_load_dwordx4 v[124:127], v6, s[16:17] offset:0 nt
	global_load_dwordx4 v[128:131], v6, s[16:17] offset:1024 nt
	global_load_dwordx4 v[132:135], v6, s[16:17] offset:2048 nt
	global_load_dwordx4 v[136:139], v6, s[16:17] offset:3072 nt
	global_load_dwordx4 v[140:143], v10, s[16:17] offset:0 nt
	global_load_dwordx4 v[144:147], v10, s[16:17] offset:1024 nt
	global_load_dwordx4 v[148:151], v10, s[16:17] offset:2048 nt
	global_load_dwordx4 v[152:155], v10, s[16:17] offset:3072 nt
	global_load_dwordx4 v[156:159], v11, s[16:17] offset:0 nt
	global_load_dwordx4 v[160:163], v11, s[16:17] offset:1024 nt
	global_load_dwordx4 v[164:167], v11, s[16:17] offset:2048 nt
	global_load_dwordx4 v[168:171], v11, s[16:17] offset:3072 nt
	global_load_dwordx4 v[172:175], v12, s[16:17] offset:0 nt
	global_load_dwordx4 v[176:179], v12, s[16:17] offset:1024 nt
	global_load_dwordx4 v[180:183], v12, s[16:17] offset:2048 nt
	global_load_dwordx4 v[184:187], v12, s[16:17] offset:3072 nt
	s_waitcnt vmcnt(47)
	v_pk_mul_f32 v[188:189], v[42:43], v[188:189]
	v_pk_mul_f32 v[190:191], v[42:43], v[190:191]
	v_pk_mul_f32 v[188:189], v[60:61], v[188:189]
	v_pk_mul_f32 v[190:191], v[62:63], v[190:191]
	global_store_dwordx4 v6, v[188:191], s[14:15] offset:0 nt
	s_waitcnt vmcnt(47)
	v_pk_mul_f32 v[192:193], v[42:43], v[192:193]
	v_pk_mul_f32 v[194:195], v[42:43], v[194:195]
	v_pk_mul_f32 v[192:193], v[64:65], v[192:193]
	v_pk_mul_f32 v[194:195], v[66:67], v[194:195]
	global_store_dwordx4 v6, v[192:195], s[14:15] offset:1024 nt
	s_waitcnt vmcnt(47)
	v_pk_mul_f32 v[196:197], v[42:43], v[196:197]
	v_pk_mul_f32 v[198:199], v[42:43], v[198:199]
	v_pk_mul_f32 v[196:197], v[68:69], v[196:197]
	v_pk_mul_f32 v[198:199], v[70:71], v[198:199]
	global_store_dwordx4 v6, v[196:199], s[14:15] offset:2048 nt
	s_waitcnt vmcnt(47)
	v_pk_mul_f32 v[200:201], v[42:43], v[200:201]
	v_pk_mul_f32 v[202:203], v[42:43], v[202:203]
	v_pk_mul_f32 v[200:201], v[72:73], v[200:201]
	v_pk_mul_f32 v[202:203], v[74:75], v[202:203]
	global_store_dwordx4 v6, v[200:203], s[14:15] offset:3072 nt
	s_waitcnt vmcnt(47)
	v_pk_mul_f32 v[204:205], v[42:43], v[204:205]
	v_pk_mul_f32 v[206:207], v[42:43], v[206:207]
	v_pk_mul_f32 v[204:205], v[76:77], v[204:205]
	v_pk_mul_f32 v[206:207], v[78:79], v[206:207]
	global_store_dwordx4 v10, v[204:207], s[14:15] offset:0 nt
	s_waitcnt vmcnt(47)
	v_pk_mul_f32 v[208:209], v[42:43], v[208:209]
	v_pk_mul_f32 v[210:211], v[42:43], v[210:211]
	v_pk_mul_f32 v[208:209], v[80:81], v[208:209]
	v_pk_mul_f32 v[210:211], v[82:83], v[210:211]
	global_store_dwordx4 v10, v[208:211], s[14:15] offset:1024 nt
	s_waitcnt vmcnt(47)
	v_pk_mul_f32 v[212:213], v[42:43], v[212:213]
	v_pk_mul_f32 v[214:215], v[42:43], v[214:215]
	v_pk_mul_f32 v[212:213], v[84:85], v[212:213]
	v_pk_mul_f32 v[214:215], v[86:87], v[214:215]
	global_store_dwordx4 v10, v[212:215], s[14:15] offset:2048 nt
	s_waitcnt vmcnt(47)
	v_pk_mul_f32 v[216:217], v[42:43], v[216:217]
	v_pk_mul_f32 v[218:219], v[42:43], v[218:219]
	v_pk_mul_f32 v[216:217], v[88:89], v[216:217]
	v_pk_mul_f32 v[218:219], v[90:91], v[218:219]
	global_store_dwordx4 v10, v[216:219], s[14:15] offset:3072 nt
	s_waitcnt vmcnt(47)
	v_pk_mul_f32 v[220:221], v[42:43], v[220:221]
	v_pk_mul_f32 v[222:223], v[42:43], v[222:223]
	v_pk_mul_f32 v[220:221], v[92:93], v[220:221]
	v_pk_mul_f32 v[222:223], v[94:95], v[222:223]
	global_store_dwordx4 v11, v[220:223], s[14:15] offset:0 nt
	s_waitcnt vmcnt(47)
; __device__ __forceinline__ float wave_sum(float v) { v = dpp_add16(v); return (rdlane(v, 0) + rdlane(v, 16)) + (rdlane(v, 32) + rdlane(v, 48)); }
; __device__ __forceinline__ void p12_peer(Frame& F) {
;     ...
;       for (int i = 0; i < 4; ++i) { const int t = F.gw + i * F.NGW;
;           const float rs = 1.0f / sqrtf(wave_sum(SSQ[i * 64 + l2_]) * (1.f / D_) + 1e-6f);
; _Pragma("nounroll")
;           for (int c0 = 0; c0 < 16; c0 += 8) {
; #pragma unroll
;               for (int c = c0; c < c0 + 8; ++c) { const size_t col = (size_t)t * D_ + (size_t)(unsigned)(256 * c + lo2_); const f32x4 gn = *(const f32x4*)(lnf + (256 * c + lo2_));
;                   const f32x4 o = *(const f32x4*)(F.out + col);
;                   *(f32x4*)(F.out + col) = (f32x4){o.x * rs * gn.x, o.y * rs * gn.y, o.z * rs * gn.z, o.w * rs * gn.w}; }
;               asm volatile("" ::: "memory"); } }
	v_pk_mul_f32 v[224:225], v[42:43], v[224:225]
	v_pk_mul_f32 v[226:227], v[42:43], v[226:227]
	v_pk_mul_f32 v[224:225], v[96:97], v[224:225]
	v_pk_mul_f32 v[226:227], v[98:99], v[226:227]
	global_store_dwordx4 v11, v[224:227], s[14:15] offset:1024 nt
	s_waitcnt vmcnt(47)
	v_pk_mul_f32 v[228:229], v[42:43], v[228:229]
	v_pk_mul_f32 v[230:231], v[42:43], v[230:231]
	v_pk_mul_f32 v[228:229], v[100:101], v[228:229]
	v_pk_mul_f32 v[230:231], v[102:103], v[230:231]
	global_store_dwordx4 v11, v[228:231], s[14:15] offset:2048 nt
	s_waitcnt vmcnt(47)
	v_pk_mul_f32 v[232:233], v[42:43], v[232:233]
	v_pk_mul_f32 v[234:235], v[42:43], v[234:235]
	v_pk_mul_f32 v[232:233], v[104:105], v[232:233]
	v_pk_mul_f32 v[234:235], v[106:107], v[234:235]
	global_store_dwordx4 v11, v[232:235], s[14:15] offset:3072 nt
	s_waitcnt vmcnt(47)
	v_pk_mul_f32 v[236:237], v[42:43], v[236:237]
	v_pk_mul_f32 v[238:239], v[42:43], v[238:239]
	v_pk_mul_f32 v[236:237], v[108:109], v[236:237]
	v_pk_mul_f32 v[238:239], v[110:111], v[238:239]
	global_store_dwordx4 v12, v[236:239], s[14:15] offset:0 nt
	s_waitcnt vmcnt(47)
	v_pk_mul_f32 v[240:241], v[42:43], v[240:241]
	v_pk_mul_f32 v[242:243], v[42:43], v[242:243]
	v_pk_mul_f32 v[240:241], v[112:113], v[240:241]
	v_pk_mul_f32 v[242:243], v[114:115], v[242:243]
	global_store_dwordx4 v12, v[240:243], s[14:15] offset:1024 nt
	s_waitcnt vmcnt(47)
	v_pk_mul_f32 v[244:245], v[42:43], v[244:245]
	v_pk_mul_f32 v[246:247], v[42:43], v[246:247]
	v_pk_mul_f32 v[244:245], v[116:117], v[244:245]
	v_pk_mul_f32 v[246:247], v[118:119], v[246:247]
	global_store_dwordx4 v12, v[244:247], s[14:15] offset:2048 nt
	s_waitcnt vmcnt(47)
	v_pk_mul_f32 v[248:249], v[42:43], v[248:249]
	v_pk_mul_f32 v[250:251], v[42:43], v[250:251]
	v_pk_mul_f32 v[248:249], v[120:121], v[248:249]
	v_pk_mul_f32 v[250:251], v[122:123], v[250:251]
	global_store_dwordx4 v12, v[248:251], s[14:15] offset:3072 nt
	s_nop 1
	global_load_dwordx4 v[188:191], v6, s[18:19] offset:0 nt
	global_load_dwordx4 v[192:195], v6, s[18:19] offset:1024 nt
	global_load_dwordx4 v[196:199], v6, s[18:19] offset:2048 nt
	global_load_dwordx4 v[200:203], v6, s[18:19] offset:3072 nt
	global_load_dwordx4 v[204:207], v10, s[18:19] offset:0 nt
	global_load_dwordx4 v[208:211], v10, s[18:19] offset:1024 nt
	global_load_dwordx4 v[212:215], v10, s[18:19] offset:2048 nt
	global_load_dwordx4 v[216:219], v10, s[18:19] offset:3072 nt
	global_load_dwordx4 v[220:223], v11, s[18:19] offset:0 nt
	global_load_dwordx4 v[224:227], v11, s[18:19] offset:1024 nt
	global_load_dwordx4 v[228:231], v11, s[18:19] offset:2048 nt
	global_load_dwordx4 v[232:235], v11, s[18:19] offset:3072 nt
	global_load_dwordx4 v[236:239], v12, s[18:19] offset:0 nt
	global_load_dwordx4 v[240:243], v12, s[18:19] offset:1024 nt
	global_load_dwordx4 v[244:247], v12, s[18:19] offset:2048 nt
	global_load_dwordx4 v[248:251], v12, s[18:19] offset:3072 nt
	s_waitcnt vmcnt(47)
	v_pk_mul_f32 v[124:125], v[44:45], v[124:125]
	v_pk_mul_f32 v[126:127], v[44:45], v[126:127]
	v_pk_mul_f32 v[124:125], v[60:61], v[124:125]
	v_pk_mul_f32 v[126:127], v[62:63], v[126:127]
	global_store_dwordx4 v6, v[124:127], s[16:17] offset:0 nt
	s_waitcnt vmcnt(47)
	v_pk_mul_f32 v[128:129], v[44:45], v[128:129]
	v_pk_mul_f32 v[130:131], v[44:45], v[130:131]
	v_pk_mul_f32 v[128:129], v[64:65], v[128:129]
	v_pk_mul_f32 v[130:131], v[66:67], v[130:131]
	global_store_dwordx4 v6, v[128:131], s[16:17] offset:1024 nt
	s_waitcnt vmcnt(47)
	v_pk_mul_f32 v[132:133], v[44:45], v[132:133]
	v_pk_mul_f32 v[134:135], v[44:45], v[134:135]
	v_pk_mul_f32 v[132:133], v[68:69], v[132:133]
	v_pk_mul_f32 v[134:135], v[70:71], v[134:135]
	global_store_dwordx4 v6, v[132:135], s[16:17] offset:2048 nt
	s_waitcnt vmcnt(47)
	v_pk_mul_f32 v[136:137], v[44:45], v[136:137]
	v_pk_mul_f32 v[138:139], v[44:45], v[138:139]
	v_pk_mul_f32 v[136:137], v[72:73], v[136:137]
	v_pk_mul_f32 v[138:139], v[74:75], v[138:139]
	global_store_dwordx4 v6, v[136:139], s[16:17] offset:3072 nt
	s_waitcnt vmcnt(47)
	v_pk_mul_f32 v[140:141], v[44:45], v[140:141]
	v_pk_mul_f32 v[142:143], v[44:45], v[142:143]
	v_pk_mul_f32 v[140:141], v[76:77], v[140:141]
	v_pk_mul_f32 v[142:143], v[78:79], v[142:143]
	global_store_dwordx4 v10, v[140:143], s[16:17] offset:0 nt
	s_waitcnt vmcnt(47)
	v_pk_mul_f32 v[144:145], v[44:45], v[144:145]
	v_pk_mul_f32 v[146:147], v[44:45], v[146:147]
	v_pk_mul_f32 v[144:145], v[80:81], v[144:145]
	v_pk_mul_f32 v[146:147], v[82:83], v[146:147]
	global_store_dwordx4 v10, v[144:147], s[16:17] offset:1024 nt
	s_waitcnt vmcnt(47)
	v_pk_mul_f32 v[148:149], v[44:45], v[148:149]
	v_pk_mul_f32 v[150:151], v[44:45], v[150:151]
	v_pk_mul_f32 v[148:149], v[84:85], v[148:149]
	v_pk_mul_f32 v[150:151], v[86:87], v[150:151]
	global_store_dwordx4 v10, v[148:151], s[16:17] offset:2048 nt
	s_waitcnt vmcnt(47)
	v_pk_mul_f32 v[152:153], v[44:45], v[152:153]
	v_pk_mul_f32 v[154:155], v[44:45], v[154:155]
	v_pk_mul_f32 v[152:153], v[88:89], v[152:153]
	v_pk_mul_f32 v[154:155], v[90:91], v[154:155]
	global_store_dwordx4 v10, v[152:155], s[16:17] offset:3072 nt
	s_waitcnt vmcnt(47)
	v_pk_mul_f32 v[156:157], v[44:45], v[156:157]
	v_pk_mul_f32 v[158:159], v[44:45], v[158:159]
	v_pk_mul_f32 v[156:157], v[92:93], v[156:157]
	v_pk_mul_f32 v[158:159], v[94:95], v[158:159]
	global_store_dwordx4 v11, v[156:159], s[16:17] offset:0 nt
	s_waitcnt vmcnt(47)
	v_pk_mul_f32 v[160:161], v[44:45], v[160:161]
	v_pk_mul_f32 v[162:163], v[44:45], v[162:163]
	v_pk_mul_f32 v[160:161], v[96:97], v[160:161]
	v_pk_mul_f32 v[162:163], v[98:99], v[162:163]
	global_store_dwordx4 v11, v[160:163], s[16:17] offset:1024 nt
	s_waitcnt vmcnt(47)
; __device__ __forceinline__ float wave_sum(float v) { v = dpp_add16(v); return (rdlane(v, 0) + rdlane(v, 16)) + (rdlane(v, 32) + rdlane(v, 48)); }
; __device__ __forceinline__ void p12_peer(Frame& F) {
;     ...
;       for (int i = 0; i < 4; ++i) { const int t = F.gw + i * F.NGW;
;           const float rs = 1.0f / sqrtf(wave_sum(SSQ[i * 64 + l2_]) * (1.f / D_) + 1e-6f);
; _Pragma("nounroll")
;           for (int c0 = 0; c0 < 16; c0 += 8) {
; #pragma unroll
;               for (int c = c0; c < c0 + 8; ++c) { const size_t col = (size_t)t * D_ + (size_t)(unsigned)(256 * c + lo2_); const f32x4 gn = *(const f32x4*)(lnf + (256 * c + lo2_));
;                   const f32x4 o = *(const f32x4*)(F.out + col);
;                   *(f32x4*)(F.out + col) = (f32x4){o.x * rs * gn.x, o.y * rs * gn.y, o.z * rs * gn.z, o.w * rs * gn.w}; }
;               asm volatile("" ::: "memory"); } }
	v_pk_mul_f32 v[164:165], v[44:45], v[164:165]
	v_pk_mul_f32 v[166:167], v[44:45], v[166:167]
	v_pk_mul_f32 v[164:165], v[100:101], v[164:165]
	v_pk_mul_f32 v[166:167], v[102:103], v[166:167]
	global_store_dwordx4 v11, v[164:167], s[16:17] offset:2048 nt
	s_waitcnt vmcnt(47)
	v_pk_mul_f32 v[168:169], v[44:45], v[168:169]
	v_pk_mul_f32 v[170:171], v[44:45], v[170:171]
	v_pk_mul_f32 v[168:169], v[104:105], v[168:169]
	v_pk_mul_f32 v[170:171], v[106:107], v[170:171]
	global_store_dwordx4 v11, v[168:171], s[16:17] offset:3072 nt
	s_waitcnt vmcnt(47)
	v_pk_mul_f32 v[172:173], v[44:45], v[172:173]
	v_pk_mul_f32 v[174:175], v[44:45], v[174:175]
	v_pk_mul_f32 v[172:173], v[108:109], v[172:173]
	v_pk_mul_f32 v[174:175], v[110:111], v[174:175]
	global_store_dwordx4 v12, v[172:175], s[16:17] offset:0 nt
	s_waitcnt vmcnt(47)
	v_pk_mul_f32 v[176:177], v[44:45], v[176:177]
	v_pk_mul_f32 v[178:179], v[44:45], v[178:179]
	v_pk_mul_f32 v[176:177], v[112:113], v[176:177]
	v_pk_mul_f32 v[178:179], v[114:115], v[178:179]
	global_store_dwordx4 v12, v[176:179], s[16:17] offset:1024 nt
	s_waitcnt vmcnt(47)
	v_pk_mul_f32 v[180:181], v[44:45], v[180:181]
	v_pk_mul_f32 v[182:183], v[44:45], v[182:183]
	v_pk_mul_f32 v[180:181], v[116:117], v[180:181]
	v_pk_mul_f32 v[182:183], v[118:119], v[182:183]
	global_store_dwordx4 v12, v[180:183], s[16:17] offset:2048 nt
	s_waitcnt vmcnt(47)
	v_pk_mul_f32 v[184:185], v[44:45], v[184:185]
	v_pk_mul_f32 v[186:187], v[44:45], v[186:187]
	v_pk_mul_f32 v[184:185], v[120:121], v[184:185]
	v_pk_mul_f32 v[186:187], v[122:123], v[186:187]
	global_store_dwordx4 v12, v[184:187], s[16:17] offset:3072 nt
	s_waitcnt vmcnt(31)
	v_pk_mul_f32 v[188:189], v[46:47], v[188:189]
	v_pk_mul_f32 v[190:191], v[46:47], v[190:191]
	v_pk_mul_f32 v[188:189], v[60:61], v[188:189]
	v_pk_mul_f32 v[190:191], v[62:63], v[190:191]
	global_store_dwordx4 v6, v[188:191], s[18:19] offset:0 nt
	s_waitcnt vmcnt(31)
	v_pk_mul_f32 v[192:193], v[46:47], v[192:193]
	v_pk_mul_f32 v[194:195], v[46:47], v[194:195]
	v_pk_mul_f32 v[192:193], v[64:65], v[192:193]
	v_pk_mul_f32 v[194:195], v[66:67], v[194:195]
	global_store_dwordx4 v6, v[192:195], s[18:19] offset:1024 nt
	s_waitcnt vmcnt(31)
	v_pk_mul_f32 v[196:197], v[46:47], v[196:197]
	v_pk_mul_f32 v[198:199], v[46:47], v[198:199]
	v_pk_mul_f32 v[196:197], v[68:69], v[196:197]
	v_pk_mul_f32 v[198:199], v[70:71], v[198:199]
	global_store_dwordx4 v6, v[196:199], s[18:19] offset:2048 nt
	s_waitcnt vmcnt(31)
	v_pk_mul_f32 v[200:201], v[46:47], v[200:201]
	v_pk_mul_f32 v[202:203], v[46:47], v[202:203]
	v_pk_mul_f32 v[200:201], v[72:73], v[200:201]
	v_pk_mul_f32 v[202:203], v[74:75], v[202:203]
	global_store_dwordx4 v6, v[200:203], s[18:19] offset:3072 nt
	s_waitcnt vmcnt(31)
	v_pk_mul_f32 v[204:205], v[46:47], v[204:205]
	v_pk_mul_f32 v[206:207], v[46:47], v[206:207]
	v_pk_mul_f32 v[204:205], v[76:77], v[204:205]
	v_pk_mul_f32 v[206:207], v[78:79], v[206:207]
	global_store_dwordx4 v10, v[204:207], s[18:19] offset:0 nt
	s_waitcnt vmcnt(31)
	v_pk_mul_f32 v[208:209], v[46:47], v[208:209]
	v_pk_mul_f32 v[210:211], v[46:47], v[210:211]
	v_pk_mul_f32 v[208:209], v[80:81], v[208:209]
	v_pk_mul_f32 v[210:211], v[82:83], v[210:211]
	global_store_dwordx4 v10, v[208:211], s[18:19] offset:1024 nt
	s_waitcnt vmcnt(31)
	v_pk_mul_f32 v[212:213], v[46:47], v[212:213]
	v_pk_mul_f32 v[214:215], v[46:47], v[214:215]
	v_pk_mul_f32 v[212:213], v[84:85], v[212:213]
	v_pk_mul_f32 v[214:215], v[86:87], v[214:215]
	global_store_dwordx4 v10, v[212:215], s[18:19] offset:2048 nt
	s_waitcnt vmcnt(31)
	v_pk_mul_f32 v[216:217], v[46:47], v[216:217]
	v_pk_mul_f32 v[218:219], v[46:47], v[218:219]
	v_pk_mul_f32 v[216:217], v[88:89], v[216:217]
	v_pk_mul_f32 v[218:219], v[90:91], v[218:219]
	global_store_dwordx4 v10, v[216:219], s[18:19] offset:3072 nt
	s_waitcnt vmcnt(31)
	v_pk_mul_f32 v[220:221], v[46:47], v[220:221]
	v_pk_mul_f32 v[222:223], v[46:47], v[222:223]
	v_pk_mul_f32 v[220:221], v[92:93], v[220:221]
	v_pk_mul_f32 v[222:223], v[94:95], v[222:223]
	global_store_dwordx4 v11, v[220:223], s[18:19] offset:0 nt
	s_waitcnt vmcnt(31)
	v_pk_mul_f32 v[224:225], v[46:47], v[224:225]
	v_pk_mul_f32 v[226:227], v[46:47], v[226:227]
	v_pk_mul_f32 v[224:225], v[96:97], v[224:225]
	v_pk_mul_f32 v[226:227], v[98:99], v[226:227]
	global_store_dwordx4 v11, v[224:227], s[18:19] offset:1024 nt
	s_waitcnt vmcnt(31)
	v_pk_mul_f32 v[228:229], v[46:47], v[228:229]
	v_pk_mul_f32 v[230:231], v[46:47], v[230:231]
	v_pk_mul_f32 v[228:229], v[100:101], v[228:229]
	v_pk_mul_f32 v[230:231], v[102:103], v[230:231]
	global_store_dwordx4 v11, v[228:231], s[18:19] offset:2048 nt
	s_waitcnt vmcnt(31)
	v_pk_mul_f32 v[232:233], v[46:47], v[232:233]
	v_pk_mul_f32 v[234:235], v[46:47], v[234:235]
	v_pk_mul_f32 v[232:233], v[104:105], v[232:233]
	v_pk_mul_f32 v[234:235], v[106:107], v[234:235]
	global_store_dwordx4 v11, v[232:235], s[18:19] offset:3072 nt
	s_waitcnt vmcnt(31)
	v_pk_mul_f32 v[236:237], v[46:47], v[236:237]
	v_pk_mul_f32 v[238:239], v[46:47], v[238:239]
	v_pk_mul_f32 v[236:237], v[108:109], v[236:237]
	v_pk_mul_f32 v[238:239], v[110:111], v[238:239]
	global_store_dwordx4 v12, v[236:239], s[18:19] offset:0 nt
	s_waitcnt vmcnt(31)
	v_pk_mul_f32 v[240:241], v[46:47], v[240:241]
	v_pk_mul_f32 v[242:243], v[46:47], v[242:243]
	v_pk_mul_f32 v[240:241], v[112:113], v[240:241]
	v_pk_mul_f32 v[242:243], v[114:115], v[242:243]
	global_store_dwordx4 v12, v[240:243], s[18:19] offset:1024 nt
	s_waitcnt vmcnt(31)
	v_pk_mul_f32 v[244:245], v[46:47], v[244:245]
	v_pk_mul_f32 v[246:247], v[46:47], v[246:247]
	v_pk_mul_f32 v[244:245], v[116:117], v[244:245]
	v_pk_mul_f32 v[246:247], v[118:119], v[246:247]
	global_store_dwordx4 v12, v[244:247], s[18:19] offset:2048 nt
	s_waitcnt vmcnt(31)
	v_pk_mul_f32 v[248:249], v[46:47], v[248:249]
	v_pk_mul_f32 v[250:251], v[46:47], v[250:251]
	v_pk_mul_f32 v[248:249], v[120:121], v[248:249]
	v_pk_mul_f32 v[250:251], v[122:123], v[250:251]
	global_store_dwordx4 v12, v[248:251], s[18:19] offset:3072 nt
